# v16 + weight-conversion loops (P2 x2, P10): counted vmcnt waits keep the next item's 16 loads in flight during the LDS transposition (was: drained to vmcnt(0) every item)
# speedup vs baseline: 1.0004x; 1.0004x over previous
.Lcva_d1:
	s_waitcnt vmcnt(0)
	s_branch .LBB0_289

.LBB0_289:
	v_add_u32_e32 v190, 0x4000, v185
	v_add_u32_e32 v191, 0x4008, v185
	v_add_u32_e32 v192, 0x4410, v185
	v_add_u32_e32 v193, 0x4418, v185
	v_add_u32_e32 v198, 0x4820, v185
	v_add_u32_e32 v199, 0x4828, v185
	v_add_u32_e32 v200, 0x4c30, v185
	v_add_u32_e32 v201, 0x4c38, v185
	v_add_u32_e32 v205, 0x5040, v185
	v_add_u32_e32 v206, 0x5048, v185
	v_add_u32_e32 v207, 0x5450, v185
	v_add_u32_e32 v208, 0x5458, v185
	v_add_u32_e32 v209, 0x5860, v185
	v_add_u32_e32 v210, 0x5868, v185
	v_add_u32_e32 v211, 0x5c70, v185
	v_add_u32_e32 v212, 0x5c78, v185
	v_add_u32_e32 v213, 0x6080, v185
	v_add_u32_e32 v214, 0x6088, v185
	v_add_u32_e32 v215, 0x6490, v185
	v_add_u32_e32 v216, 0x6498, v185
	v_add_u32_e32 v217, 0x68a0, v185
	v_add_u32_e32 v218, 0x68a8, v185
	v_add_u32_e32 v219, 0x6cb0, v185
	v_add_u32_e32 v220, 0x6cb8, v185
	v_add_u32_e32 v221, 0x70c0, v185
	v_add_u32_e32 v222, 0x70c8, v185
	v_add_u32_e32 v223, 0x74d0, v185
	v_add_u32_e32 v224, 0x74d8, v185
	v_add_u32_e32 v225, 0x78e0, v185
	v_add_u32_e32 v226, 0x78e8, v185
	v_add_u32_e32 v227, 0x7cf0, v185
	v_add_u32_e32 v228, 0x7cf8, v185
	s_waitcnt vmcnt(31)
	ds_write2_b32 v190, v2, v3 offset1:1
	ds_write2_b32 v191, v4, v5 offset1:1
	s_waitcnt vmcnt(30)
	ds_write2_b32 v192, v6, v7 offset1:1
	ds_write2_b32 v193, v8, v9 offset1:1
	s_waitcnt vmcnt(29)
	ds_write2_b32 v198, v10, v11 offset1:1
	ds_write2_b32 v199, v12, v13 offset1:1
	s_waitcnt vmcnt(28)
	ds_write2_b32 v200, v14, v15 offset1:1
	ds_write2_b32 v201, v16, v17 offset1:1
	s_waitcnt vmcnt(27)
	ds_write2_b32 v205, v18, v19 offset1:1
	ds_write2_b32 v206, v20, v21 offset1:1
	s_waitcnt vmcnt(26)
	ds_write2_b32 v207, v22, v23 offset1:1
	ds_write2_b32 v208, v24, v25 offset1:1
	s_waitcnt vmcnt(25)
	ds_write2_b32 v209, v26, v27 offset1:1
	ds_write2_b32 v210, v28, v29 offset1:1
	s_waitcnt vmcnt(24)
	ds_write2_b32 v211, v30, v31 offset1:1
	ds_write2_b32 v212, v32, v33 offset1:1
	s_waitcnt vmcnt(23)
	ds_write2_b32 v213, v34, v35 offset1:1
	ds_write2_b32 v214, v36, v37 offset1:1
	s_waitcnt vmcnt(22)
	ds_write2_b32 v215, v38, v39 offset1:1
	ds_write2_b32 v216, v40, v41 offset1:1
	s_waitcnt vmcnt(21)
	ds_write2_b32 v217, v42, v43 offset1:1
	ds_write2_b32 v218, v44, v45 offset1:1
	s_waitcnt vmcnt(20)
	ds_write2_b32 v219, v46, v47 offset1:1
	ds_write2_b32 v220, v48, v49 offset1:1
	s_waitcnt vmcnt(19)
	ds_write2_b32 v221, v50, v51 offset1:1
	ds_write2_b32 v222, v52, v53 offset1:1
	s_waitcnt vmcnt(18)
	ds_write2_b32 v223, v54, v55 offset1:1
	ds_write2_b32 v224, v56, v57 offset1:1
	s_waitcnt vmcnt(17)
	ds_write2_b32 v225, v74, v75 offset1:1
	ds_write2_b32 v226, v76, v77 offset1:1
	s_waitcnt vmcnt(16)
	ds_write2_b32 v227, v78, v79 offset1:1
	ds_write2_b32 v228, v80, v81 offset1:1
	s_waitcnt lgkmcnt(0)
	ds_read_b32 v132, v184 offset:16384
	v_cmp_eq_f32_e64 s[20:21], s34, 0
	s_and_b64 vcc, exec, s[20:21]
	v_add_u32_e32 v188, 0x4000, v184
	v_add_u32_e32 v189, 0x4200, v184
	v_add_u32_e32 v187, 0x4400, v184
	s_cbranch_vccnz .LBB0_310
	ds_read2_b32 v[154:155], v188 offset0:56 offset1:65
	ds_read2_b32 v[156:157], v188 offset0:121 offset1:130
	ds_read2_b32 v[158:159], v188 offset0:186 offset1:195
	s_waitcnt lgkmcnt(3)
	v_mul_f32_e32 v160, s34, v132
	v_med3_f32 v160, v160, s62, v186
	s_waitcnt lgkmcnt(2)
	v_mul_f32_e32 v155, s34, v155
	v_med3_f32 v155, v155, s62, v186
	v_mov_b32_e32 v230, v133
	v_cvt_pk_fp8_f32 v230, v160, v155
	ds_read2_b32 v[174:175], v189 offset0:123 offset1:132
	ds_read2_b32 v[160:161], v187 offset0:60 offset1:69
	ds_read2_b32 v[172:173], v187 offset0:125 offset1:134
	s_waitcnt lgkmcnt(4)
	v_mul_f32_e32 v157, s34, v157
	s_waitcnt lgkmcnt(3)
	v_mul_f32_e32 v159, s34, v159
	v_med3_f32 v157, v157, s62, v186
	v_med3_f32 v155, v159, s62, v186
	ds_read2_b32 v[178:179], v187 offset0:190 offset1:199
	v_cvt_pk_fp8_f32 v230, v157, v155 op_sel:[0,0,1]
	s_waitcnt lgkmcnt(3)
	v_mul_f32_e32 v155, s34, v175
	s_waitcnt lgkmcnt(2)
	v_mul_f32_e32 v157, s34, v161
	v_med3_f32 v155, v155, s62, v186
	v_med3_f32 v157, v157, s62, v186
	v_mov_b32_e32 v231, v133
	v_cvt_pk_fp8_f32 v231, v155, v157
	s_waitcnt lgkmcnt(1)
	v_mul_f32_e32 v159, s34, v173
	s_waitcnt lgkmcnt(0)
	v_mul_f32_e32 v155, s34, v179
	v_med3_f32 v157, v159, s62, v186
	v_med3_f32 v155, v155, s62, v186
	v_cvt_pk_fp8_f32 v231, v157, v155 op_sel:[0,0,1]
	ds_read2_b32 v[234:235], v188 offset0:8 offset1:16
	ds_read2_b32 v[236:237], v188 offset0:73 offset1:81
	ds_read2_b32 v[238:239], v188 offset0:138 offset1:146
	ds_read2_b32 v[240:241], v188 offset0:203 offset1:211
	v_mov_b64_e32 v[176:177], s[0:1]
	v_mad_u64_u32 v[232:233], s[20:21], s26, v134, v[176:177]
	v_lshl_add_u64 v[232:233], v[232:233], 0, v[136:137]
	s_waitcnt lgkmcnt(3)
	v_mul_f32_e32 v155, s34, v234
	s_waitcnt lgkmcnt(2)
	v_mul_f32_e32 v157, s34, v236
	global_store_dwordx2 v[232:233], v[230:231], off nt
	v_med3_f32 v155, v155, s62, v186
	v_med3_f32 v157, v157, s62, v186
	v_mov_b32_e32 v230, v133
	v_cvt_pk_fp8_f32 v230, v155, v157
	ds_read2_b32 v[232:233], v187 offset0:12 offset1:20
	ds_read2_b32 v[242:243], v187 offset0:77 offset1:85
	ds_read2_b32 v[244:245], v187 offset0:142 offset1:150
	s_waitcnt lgkmcnt(4)
	v_mul_f32_e32 v159, s34, v238
	s_waitcnt lgkmcnt(3)
	v_mul_f32_e32 v161, s34, v240
	v_med3_f32 v159, v159, s62, v186
	v_med3_f32 v155, v161, s62, v186
	ds_read2_b32 v[246:247], v187 offset0:207 offset1:215
	v_cvt_pk_fp8_f32 v230, v159, v155 op_sel:[0,0,1]
	s_waitcnt lgkmcnt(3)
	v_mul_f32_e32 v155, s34, v232
	s_waitcnt lgkmcnt(2)
	v_mul_f32_e32 v157, s34, v242
	v_med3_f32 v155, v155, s62, v186
	v_med3_f32 v157, v157, s62, v186
	v_mov_b32_e32 v231, v133
	v_cvt_pk_fp8_f32 v231, v155, v157
	s_waitcnt lgkmcnt(1)
	v_mul_f32_e32 v159, s34, v244
	s_waitcnt lgkmcnt(0)
	v_mul_f32_e32 v155, s34, v246
	v_med3_f32 v157, v159, s62, v186
	v_med3_f32 v155, v155, s62, v186
	v_cvt_pk_fp8_f32 v231, v157, v155 op_sel:[0,0,1]
	v_mad_u64_u32 v[248:249], s[20:21], s26, v138, v[176:177]
	v_lshl_add_u64 v[248:249], v[248:249], 0, v[136:137]
	v_mul_f32_e32 v155, s34, v235
	v_mul_f32_e32 v157, s34, v237
	global_store_dwordx2 v[248:249], v[230:231], off nt
	v_med3_f32 v155, v155, s62, v186
	v_med3_f32 v157, v157, s62, v186
	v_mov_b32_e32 v230, v133
	v_cvt_pk_fp8_f32 v230, v155, v157
	v_mul_f32_e32 v159, s34, v239
	v_mul_f32_e32 v155, s34, v241
	v_med3_f32 v157, v159, s62, v186
	v_med3_f32 v155, v155, s62, v186
	v_cvt_pk_fp8_f32 v230, v157, v155 op_sel:[0,0,1]
	v_mul_f32_e32 v155, s34, v233
	v_mul_f32_e32 v157, s34, v243
	v_med3_f32 v155, v155, s62, v186
	v_med3_f32 v157, v157, s62, v186
	v_mov_b32_e32 v231, v133
	v_cvt_pk_fp8_f32 v231, v155, v157
	v_mul_f32_e32 v159, s34, v245
	v_mul_f32_e32 v155, s34, v247
	v_med3_f32 v157, v159, s62, v186
	v_med3_f32 v155, v155, s62, v186
	v_cvt_pk_fp8_f32 v231, v157, v155 op_sel:[0,0,1]
	ds_read2_b32 v[234:235], v188 offset0:24 offset1:32
	ds_read2_b32 v[236:237], v188 offset0:89 offset1:97
	ds_read2_b32 v[238:239], v188 offset0:154 offset1:162
	ds_read2_b32 v[240:241], v188 offset0:219 offset1:227
	v_mad_u64_u32 v[232:233], s[20:21], s26, v140, v[176:177]
	v_lshl_add_u64 v[232:233], v[232:233], 0, v[136:137]
	s_waitcnt lgkmcnt(3)
	v_mul_f32_e32 v155, s34, v234
	s_waitcnt lgkmcnt(2)
	v_mul_f32_e32 v157, s34, v236
	global_store_dwordx2 v[232:233], v[230:231], off nt
	v_med3_f32 v155, v155, s62, v186
	v_med3_f32 v157, v157, s62, v186
	v_mov_b32_e32 v230, v133
	v_cvt_pk_fp8_f32 v230, v155, v157
	ds_read2_b32 v[232:233], v187 offset0:28 offset1:36
	ds_read2_b32 v[242:243], v187 offset0:93 offset1:101
	ds_read2_b32 v[244:245], v187 offset0:158 offset1:166
	s_waitcnt lgkmcnt(4)
	v_mul_f32_e32 v159, s34, v238
	s_waitcnt lgkmcnt(3)
	v_mul_f32_e32 v161, s34, v240
	v_med3_f32 v159, v159, s62, v186
	v_med3_f32 v155, v161, s62, v186
	ds_read2_b32 v[246:247], v187 offset0:223 offset1:231
	v_cvt_pk_fp8_f32 v230, v159, v155 op_sel:[0,0,1]
	s_waitcnt lgkmcnt(3)
	v_mul_f32_e32 v155, s34, v232
	s_waitcnt lgkmcnt(2)
	v_mul_f32_e32 v157, s34, v242
	v_med3_f32 v155, v155, s62, v186
	v_med3_f32 v157, v157, s62, v186
	v_mov_b32_e32 v231, v133
	v_cvt_pk_fp8_f32 v231, v155, v157
	s_waitcnt lgkmcnt(1)
	v_mul_f32_e32 v159, s34, v244
	s_waitcnt lgkmcnt(0)
	v_mul_f32_e32 v155, s34, v246
	v_med3_f32 v157, v159, s62, v186
	v_med3_f32 v155, v155, s62, v186
	v_cvt_pk_fp8_f32 v231, v157, v155 op_sel:[0,0,1]
	v_mad_u64_u32 v[248:249], s[20:21], s26, v142, v[176:177]
	v_lshl_add_u64 v[248:249], v[248:249], 0, v[136:137]
	v_mul_f32_e32 v155, s34, v235
	v_mul_f32_e32 v157, s34, v237
	global_store_dwordx2 v[248:249], v[230:231], off nt
	v_med3_f32 v155, v155, s62, v186
	v_med3_f32 v157, v157, s62, v186
	v_mov_b32_e32 v230, v133
	v_cvt_pk_fp8_f32 v230, v155, v157
	v_mul_f32_e32 v159, s34, v239
	v_mul_f32_e32 v155, s34, v241
	v_med3_f32 v157, v159, s62, v186
	v_med3_f32 v155, v155, s62, v186
	v_cvt_pk_fp8_f32 v230, v157, v155 op_sel:[0,0,1]
	v_mul_f32_e32 v155, s34, v233
	v_mul_f32_e32 v157, s34, v243
	v_med3_f32 v155, v155, s62, v186
	v_med3_f32 v157, v157, s62, v186
	v_mov_b32_e32 v231, v133
	v_cvt_pk_fp8_f32 v231, v155, v157
	v_mul_f32_e32 v159, s34, v245
	v_mul_f32_e32 v155, s34, v247
	v_med3_f32 v157, v159, s62, v186
	v_med3_f32 v155, v155, s62, v186
	v_cvt_pk_fp8_f32 v231, v157, v155 op_sel:[0,0,1]
	ds_read2_b32 v[234:235], v188 offset0:40 offset1:48
	ds_read2_b32 v[236:237], v188 offset0:105 offset1:113
	ds_read2_b32 v[238:239], v188 offset0:170 offset1:178
	ds_read2_b32 v[240:241], v188 offset0:235 offset1:243
	v_mad_u64_u32 v[232:233], s[20:21], s26, v144, v[176:177]
	v_lshl_add_u64 v[232:233], v[232:233], 0, v[136:137]
	s_waitcnt lgkmcnt(3)
	v_mul_f32_e32 v155, s34, v234
	s_waitcnt lgkmcnt(2)
	v_mul_f32_e32 v157, s34, v236
	global_store_dwordx2 v[232:233], v[230:231], off nt
	v_med3_f32 v155, v155, s62, v186
	v_med3_f32 v157, v157, s62, v186
	v_mov_b32_e32 v230, v133
	v_cvt_pk_fp8_f32 v230, v155, v157
	ds_read2_b32 v[232:233], v187 offset0:44 offset1:52
	ds_read2_b32 v[242:243], v187 offset0:109 offset1:117
	ds_read2_b32 v[244:245], v187 offset0:174 offset1:182
	s_waitcnt lgkmcnt(4)
	v_mul_f32_e32 v159, s34, v238
	s_waitcnt lgkmcnt(3)
	v_mul_f32_e32 v161, s34, v240
	v_med3_f32 v159, v159, s62, v186
	v_med3_f32 v155, v161, s62, v186
	ds_read2_b32 v[246:247], v187 offset0:239 offset1:247
	v_cvt_pk_fp8_f32 v230, v159, v155 op_sel:[0,0,1]
	s_waitcnt lgkmcnt(3)
	v_mul_f32_e32 v155, s34, v232
	s_waitcnt lgkmcnt(2)
	v_mul_f32_e32 v157, s34, v242
	v_med3_f32 v155, v155, s62, v186
	v_med3_f32 v157, v157, s62, v186
	v_mov_b32_e32 v231, v133
	v_cvt_pk_fp8_f32 v231, v155, v157
	s_waitcnt lgkmcnt(1)
	v_mul_f32_e32 v159, s34, v244
	s_waitcnt lgkmcnt(0)
	v_mul_f32_e32 v155, s34, v246
	v_med3_f32 v157, v159, s62, v186
	v_med3_f32 v155, v155, s62, v186
	v_cvt_pk_fp8_f32 v231, v157, v155 op_sel:[0,0,1]
	v_mad_u64_u32 v[248:249], s[20:21], s26, v146, v[176:177]
	v_lshl_add_u64 v[248:249], v[248:249], 0, v[136:137]
	v_mul_f32_e32 v155, s34, v235
	v_mul_f32_e32 v157, s34, v237
	global_store_dwordx2 v[248:249], v[230:231], off nt
	v_med3_f32 v155, v155, s62, v186
	v_med3_f32 v157, v157, s62, v186
	v_mov_b32_e32 v230, v133
	v_cvt_pk_fp8_f32 v230, v155, v157
	v_mul_f32_e32 v159, s34, v239
	v_mul_f32_e32 v155, s34, v241
	v_med3_f32 v157, v159, s62, v186
	v_med3_f32 v155, v155, s62, v186
	v_cvt_pk_fp8_f32 v230, v157, v155 op_sel:[0,0,1]
	v_mul_f32_e32 v155, s34, v233
	v_mul_f32_e32 v157, s34, v243
	v_med3_f32 v155, v155, s62, v186
	v_med3_f32 v157, v157, s62, v186
	v_mov_b32_e32 v231, v133
	v_cvt_pk_fp8_f32 v231, v155, v157
	v_mul_f32_e32 v159, s34, v245
	v_mul_f32_e32 v155, s34, v247
	v_med3_f32 v157, v159, s62, v186
	v_med3_f32 v155, v155, s62, v186
	v_cvt_pk_fp8_f32 v231, v157, v155 op_sel:[0,0,1]
	v_mul_f32_e32 v154, s34, v154
	v_mul_f32_e32 v155, s34, v156
	v_med3_f32 v157, v154, s62, v186
	v_med3_f32 v155, v155, s62, v186
	v_mov_b32_e32 v154, v133
	v_cvt_pk_fp8_f32 v154, v157, v155
	v_mul_f32_e32 v156, s34, v158
	v_mul_f32_e32 v155, s34, v174
	v_med3_f32 v156, v156, s62, v186
	v_med3_f32 v155, v155, s62, v186
	ds_read_b32 v158, v184 offset:18428
	v_cvt_pk_fp8_f32 v154, v156, v155 op_sel:[0,0,1]
	v_mul_f32_e32 v155, s34, v160
	v_mul_f32_e32 v156, s34, v172
	v_med3_f32 v159, v155, s62, v186
	v_med3_f32 v156, v156, s62, v186
	v_mov_b32_e32 v155, v133
	v_cvt_pk_fp8_f32 v155, v159, v156
	v_mul_f32_e32 v157, s34, v178
	s_waitcnt lgkmcnt(0)
	v_mul_f32_e32 v156, s34, v158
	v_med3_f32 v157, v157, s62, v186
	v_med3_f32 v156, v156, s62, v186
	v_cvt_pk_fp8_f32 v155, v157, v156 op_sel:[0,0,1]
	v_mad_u64_u32 v[232:233], s[20:21], s26, v148, v[176:177]
	v_mad_u64_u32 v[156:157], s[20:21], s26, v150, v[176:177]
	v_lshl_add_u64 v[232:233], v[232:233], 0, v[136:137]
	v_lshl_add_u64 v[156:157], v[156:157], 0, v[136:137]
	global_store_dwordx2 v[232:233], v[230:231], off nt
	global_store_dwordx2 v[156:157], v[154:155], off nt
	s_cbranch_execnz .LBB0_292

.LBB0_326:
	s_waitcnt vmcnt(31)
	ds_write2_b32 v190, v62, v63 offset1:1
	ds_write2_b32 v191, v64, v65 offset1:1
	s_waitcnt vmcnt(30)
	ds_write2_b32 v192, v58, v59 offset1:1
	ds_write2_b32 v193, v60, v61 offset1:1
	s_waitcnt vmcnt(29)
	ds_write2_b32 v198, v70, v71 offset1:1
	ds_write2_b32 v199, v72, v73 offset1:1
	s_waitcnt vmcnt(28)
	ds_write2_b32 v200, v66, v67 offset1:1
	ds_write2_b32 v201, v68, v69 offset1:1
	s_waitcnt vmcnt(27)
	ds_write2_b32 v205, v86, v87 offset1:1
	ds_write2_b32 v206, v88, v89 offset1:1
	s_waitcnt vmcnt(26)
	ds_write2_b32 v207, v82, v83 offset1:1
	ds_write2_b32 v208, v84, v85 offset1:1
	s_waitcnt vmcnt(25)
	ds_write2_b32 v209, v94, v95 offset1:1
	ds_write2_b32 v210, v96, v97 offset1:1
	s_waitcnt vmcnt(24)
	ds_write2_b32 v211, v90, v91 offset1:1
	ds_write2_b32 v212, v92, v93 offset1:1
	s_waitcnt vmcnt(23)
	ds_write2_b32 v213, v102, v103 offset1:1
	ds_write2_b32 v214, v104, v105 offset1:1
	s_waitcnt vmcnt(22)
	ds_write2_b32 v215, v98, v99 offset1:1
	ds_write2_b32 v216, v100, v101 offset1:1
	s_waitcnt vmcnt(21)
	ds_write2_b32 v217, v110, v111 offset1:1
	ds_write2_b32 v218, v112, v113 offset1:1
	s_waitcnt vmcnt(20)
	ds_write2_b32 v219, v106, v107 offset1:1
	ds_write2_b32 v220, v108, v109 offset1:1
	s_waitcnt vmcnt(19)
	ds_write2_b32 v221, v118, v119 offset1:1
	ds_write2_b32 v222, v120, v121 offset1:1
	s_waitcnt vmcnt(18)
	ds_write2_b32 v223, v114, v115 offset1:1
	ds_write2_b32 v224, v116, v117 offset1:1
	s_waitcnt vmcnt(17)
	ds_write2_b32 v225, v126, v127 offset1:1
	ds_write2_b32 v226, v128, v129 offset1:1
	s_waitcnt vmcnt(16)
	ds_write2_b32 v227, v122, v123 offset1:1
	ds_write2_b32 v228, v124, v125 offset1:1
	s_waitcnt lgkmcnt(0)
	s_waitcnt lgkmcnt(14)
	ds_read_b32 v132, v184 offset:16384
	v_cmp_eq_f32_e64 s[18:19], s66, 0
	s_and_b64 vcc, exec, s[18:19]
	s_cbranch_vccnz .LBB0_328
	ds_read2_b32 v[154:155], v188 offset0:56 offset1:65
	ds_read2_b32 v[156:157], v188 offset0:121 offset1:130
	ds_read2_b32 v[158:159], v188 offset0:186 offset1:195
	s_waitcnt lgkmcnt(3)
	v_mul_f32_e32 v160, s66, v132
	v_med3_f32 v160, v160, s62, v186
	s_waitcnt lgkmcnt(2)
	v_mul_f32_e32 v155, s66, v155
	v_med3_f32 v155, v155, s62, v186
	v_mov_b32_e32 v190, v133
	v_cvt_pk_fp8_f32 v190, v160, v155
	ds_read2_b32 v[174:175], v189 offset0:123 offset1:132
	ds_read2_b32 v[160:161], v187 offset0:60 offset1:69
	ds_read2_b32 v[172:173], v187 offset0:125 offset1:134
	s_waitcnt lgkmcnt(4)
	v_mul_f32_e32 v157, s66, v157
	s_waitcnt lgkmcnt(3)
	v_mul_f32_e32 v159, s66, v159
	v_med3_f32 v157, v157, s62, v186
	v_med3_f32 v155, v159, s62, v186
	ds_read2_b32 v[178:179], v187 offset0:190 offset1:199
	v_cvt_pk_fp8_f32 v190, v157, v155 op_sel:[0,0,1]
	s_waitcnt lgkmcnt(3)
	v_mul_f32_e32 v155, s66, v175
	s_waitcnt lgkmcnt(2)
	v_mul_f32_e32 v157, s66, v161
	v_med3_f32 v155, v155, s62, v186
	v_med3_f32 v157, v157, s62, v186
	v_mov_b32_e32 v191, v133
	v_cvt_pk_fp8_f32 v191, v155, v157
	s_waitcnt lgkmcnt(1)
	v_mul_f32_e32 v159, s66, v173
	s_waitcnt lgkmcnt(0)
	v_mul_f32_e32 v155, s66, v179
	v_med3_f32 v157, v159, s62, v186
	v_med3_f32 v155, v155, s62, v186
	v_cvt_pk_fp8_f32 v191, v157, v155 op_sel:[0,0,1]
	ds_read2_b32 v[198:199], v188 offset0:8 offset1:16
	ds_read2_b32 v[200:201], v188 offset0:73 offset1:81
	ds_read2_b32 v[206:207], v188 offset0:138 offset1:146
	ds_read2_b32 v[208:209], v188 offset0:203 offset1:211
	v_mov_b64_e32 v[176:177], s[16:17]
	v_mad_u64_u32 v[192:193], s[18:19], s65, v134, v[176:177]
	v_lshl_add_u64 v[192:193], v[192:193], 0, v[136:137]
	s_waitcnt lgkmcnt(3)
	v_mul_f32_e32 v155, s66, v198
	s_waitcnt lgkmcnt(2)
	v_mul_f32_e32 v157, s66, v200
	global_store_dwordx2 v[192:193], v[190:191], off nt
	v_med3_f32 v155, v155, s62, v186
	v_med3_f32 v157, v157, s62, v186
	v_mov_b32_e32 v190, v133
	v_cvt_pk_fp8_f32 v190, v155, v157
	ds_read2_b32 v[192:193], v187 offset0:12 offset1:20
	ds_read2_b32 v[210:211], v187 offset0:77 offset1:85
	ds_read2_b32 v[212:213], v187 offset0:142 offset1:150
	s_waitcnt lgkmcnt(4)
	v_mul_f32_e32 v159, s66, v206
	s_waitcnt lgkmcnt(3)
	v_mul_f32_e32 v161, s66, v208
	v_med3_f32 v159, v159, s62, v186
	v_med3_f32 v155, v161, s62, v186
	ds_read2_b32 v[214:215], v187 offset0:207 offset1:215
	v_cvt_pk_fp8_f32 v190, v159, v155 op_sel:[0,0,1]
	s_waitcnt lgkmcnt(3)
	v_mul_f32_e32 v155, s66, v192
	s_waitcnt lgkmcnt(2)
	v_mul_f32_e32 v157, s66, v210
	v_med3_f32 v155, v155, s62, v186
	v_med3_f32 v157, v157, s62, v186
	v_mov_b32_e32 v191, v133
	v_cvt_pk_fp8_f32 v191, v155, v157
	s_waitcnt lgkmcnt(1)
	v_mul_f32_e32 v159, s66, v212
	s_waitcnt lgkmcnt(0)
	v_mul_f32_e32 v155, s66, v214
	v_med3_f32 v157, v159, s62, v186
	v_med3_f32 v155, v155, s62, v186
	v_cvt_pk_fp8_f32 v191, v157, v155 op_sel:[0,0,1]
	v_mad_u64_u32 v[216:217], s[18:19], s65, v138, v[176:177]
	v_lshl_add_u64 v[216:217], v[216:217], 0, v[136:137]
	v_mul_f32_e32 v155, s66, v199
	v_mul_f32_e32 v157, s66, v201
	global_store_dwordx2 v[216:217], v[190:191], off nt
	v_med3_f32 v155, v155, s62, v186
	v_med3_f32 v157, v157, s62, v186
	v_mov_b32_e32 v190, v133
	v_cvt_pk_fp8_f32 v190, v155, v157
	v_mul_f32_e32 v159, s66, v207
	v_mul_f32_e32 v155, s66, v209
	v_med3_f32 v157, v159, s62, v186
	v_med3_f32 v155, v155, s62, v186
	v_cvt_pk_fp8_f32 v190, v157, v155 op_sel:[0,0,1]
	v_mul_f32_e32 v155, s66, v193
	v_mul_f32_e32 v157, s66, v211
	v_med3_f32 v155, v155, s62, v186
	v_med3_f32 v157, v157, s62, v186
	v_mov_b32_e32 v191, v133
	v_cvt_pk_fp8_f32 v191, v155, v157
	v_mul_f32_e32 v159, s66, v213
	v_mul_f32_e32 v155, s66, v215
	v_med3_f32 v157, v159, s62, v186
	v_med3_f32 v155, v155, s62, v186
	v_cvt_pk_fp8_f32 v191, v157, v155 op_sel:[0,0,1]
	ds_read2_b32 v[198:199], v188 offset0:24 offset1:32
	ds_read2_b32 v[200:201], v188 offset0:89 offset1:97
	ds_read2_b32 v[206:207], v188 offset0:154 offset1:162
	ds_read2_b32 v[208:209], v188 offset0:219 offset1:227
	v_mad_u64_u32 v[192:193], s[18:19], s65, v140, v[176:177]
	v_lshl_add_u64 v[192:193], v[192:193], 0, v[136:137]
	s_waitcnt lgkmcnt(3)
	v_mul_f32_e32 v155, s66, v198
	s_waitcnt lgkmcnt(2)
	v_mul_f32_e32 v157, s66, v200
	global_store_dwordx2 v[192:193], v[190:191], off nt
	v_med3_f32 v155, v155, s62, v186
	v_med3_f32 v157, v157, s62, v186
	v_mov_b32_e32 v190, v133
	v_cvt_pk_fp8_f32 v190, v155, v157
	ds_read2_b32 v[192:193], v187 offset0:28 offset1:36
	ds_read2_b32 v[210:211], v187 offset0:93 offset1:101
	ds_read2_b32 v[212:213], v187 offset0:158 offset1:166
	s_waitcnt lgkmcnt(4)
	v_mul_f32_e32 v159, s66, v206
	s_waitcnt lgkmcnt(3)
	v_mul_f32_e32 v161, s66, v208
	v_med3_f32 v159, v159, s62, v186
	v_med3_f32 v155, v161, s62, v186
	ds_read2_b32 v[214:215], v187 offset0:223 offset1:231
	v_cvt_pk_fp8_f32 v190, v159, v155 op_sel:[0,0,1]
	s_waitcnt lgkmcnt(3)
	v_mul_f32_e32 v155, s66, v192
	s_waitcnt lgkmcnt(2)
	v_mul_f32_e32 v157, s66, v210
	v_med3_f32 v155, v155, s62, v186
	v_med3_f32 v157, v157, s62, v186
	v_mov_b32_e32 v191, v133
	v_cvt_pk_fp8_f32 v191, v155, v157
	s_waitcnt lgkmcnt(1)
	v_mul_f32_e32 v159, s66, v212
	s_waitcnt lgkmcnt(0)
	v_mul_f32_e32 v155, s66, v214
	v_med3_f32 v157, v159, s62, v186
	v_med3_f32 v155, v155, s62, v186
	v_cvt_pk_fp8_f32 v191, v157, v155 op_sel:[0,0,1]
	v_mad_u64_u32 v[216:217], s[18:19], s65, v142, v[176:177]
	v_lshl_add_u64 v[216:217], v[216:217], 0, v[136:137]
	v_mul_f32_e32 v155, s66, v199
	v_mul_f32_e32 v157, s66, v201
	global_store_dwordx2 v[216:217], v[190:191], off nt
	v_med3_f32 v155, v155, s62, v186
	v_med3_f32 v157, v157, s62, v186
	v_mov_b32_e32 v190, v133
	v_cvt_pk_fp8_f32 v190, v155, v157
	v_mul_f32_e32 v159, s66, v207
	v_mul_f32_e32 v155, s66, v209
	v_med3_f32 v157, v159, s62, v186
	v_med3_f32 v155, v155, s62, v186
	v_cvt_pk_fp8_f32 v190, v157, v155 op_sel:[0,0,1]
	v_mul_f32_e32 v155, s66, v193
	v_mul_f32_e32 v157, s66, v211
	v_med3_f32 v155, v155, s62, v186
	v_med3_f32 v157, v157, s62, v186
	v_mov_b32_e32 v191, v133
	v_cvt_pk_fp8_f32 v191, v155, v157
	v_mul_f32_e32 v159, s66, v213
	v_mul_f32_e32 v155, s66, v215
	v_med3_f32 v157, v159, s62, v186
	v_med3_f32 v155, v155, s62, v186
	v_cvt_pk_fp8_f32 v191, v157, v155 op_sel:[0,0,1]
	ds_read2_b32 v[198:199], v188 offset0:40 offset1:48
	ds_read2_b32 v[200:201], v188 offset0:105 offset1:113
	ds_read2_b32 v[206:207], v188 offset0:170 offset1:178
	ds_read2_b32 v[208:209], v188 offset0:235 offset1:243
	v_mad_u64_u32 v[192:193], s[18:19], s65, v144, v[176:177]
	v_lshl_add_u64 v[192:193], v[192:193], 0, v[136:137]
	s_waitcnt lgkmcnt(3)
	v_mul_f32_e32 v155, s66, v198
	s_waitcnt lgkmcnt(2)
	v_mul_f32_e32 v157, s66, v200
	global_store_dwordx2 v[192:193], v[190:191], off nt
	v_med3_f32 v155, v155, s62, v186
	v_med3_f32 v157, v157, s62, v186
	v_mov_b32_e32 v190, v133
	v_cvt_pk_fp8_f32 v190, v155, v157
	ds_read2_b32 v[192:193], v187 offset0:44 offset1:52
	ds_read2_b32 v[210:211], v187 offset0:109 offset1:117
	ds_read2_b32 v[212:213], v187 offset0:174 offset1:182
	s_waitcnt lgkmcnt(4)
	v_mul_f32_e32 v159, s66, v206
	s_waitcnt lgkmcnt(3)
	v_mul_f32_e32 v161, s66, v208
	v_med3_f32 v159, v159, s62, v186
	v_med3_f32 v155, v161, s62, v186
	ds_read2_b32 v[214:215], v187 offset0:239 offset1:247
	v_cvt_pk_fp8_f32 v190, v159, v155 op_sel:[0,0,1]
	s_waitcnt lgkmcnt(3)
	v_mul_f32_e32 v155, s66, v192
	s_waitcnt lgkmcnt(2)
	v_mul_f32_e32 v157, s66, v210
	v_med3_f32 v155, v155, s62, v186
	v_med3_f32 v157, v157, s62, v186
	v_mov_b32_e32 v191, v133
	v_cvt_pk_fp8_f32 v191, v155, v157
	s_waitcnt lgkmcnt(1)
	v_mul_f32_e32 v159, s66, v212
	s_waitcnt lgkmcnt(0)
	v_mul_f32_e32 v155, s66, v214
	v_med3_f32 v157, v159, s62, v186
	v_med3_f32 v155, v155, s62, v186
	v_cvt_pk_fp8_f32 v191, v157, v155 op_sel:[0,0,1]
	v_mad_u64_u32 v[216:217], s[18:19], s65, v146, v[176:177]
	v_lshl_add_u64 v[216:217], v[216:217], 0, v[136:137]
	v_mul_f32_e32 v155, s66, v199
	v_mul_f32_e32 v157, s66, v201
	global_store_dwordx2 v[216:217], v[190:191], off nt
	v_med3_f32 v155, v155, s62, v186
	v_med3_f32 v157, v157, s62, v186
	v_mov_b32_e32 v190, v133
	v_cvt_pk_fp8_f32 v190, v155, v157
	v_mul_f32_e32 v159, s66, v207
	v_mul_f32_e32 v155, s66, v209
	v_med3_f32 v157, v159, s62, v186
	v_med3_f32 v155, v155, s62, v186
	v_cvt_pk_fp8_f32 v190, v157, v155 op_sel:[0,0,1]
	v_mul_f32_e32 v155, s66, v193
	v_mul_f32_e32 v157, s66, v211
	v_med3_f32 v155, v155, s62, v186
	v_med3_f32 v157, v157, s62, v186
	v_mov_b32_e32 v191, v133
	v_cvt_pk_fp8_f32 v191, v155, v157
	v_mul_f32_e32 v159, s66, v213
	v_mul_f32_e32 v155, s66, v215
	v_med3_f32 v157, v159, s62, v186
	v_med3_f32 v155, v155, s62, v186
	v_cvt_pk_fp8_f32 v191, v157, v155 op_sel:[0,0,1]
	v_mul_f32_e32 v154, s66, v154
	v_mul_f32_e32 v155, s66, v156
	v_med3_f32 v157, v154, s62, v186
	v_med3_f32 v155, v155, s62, v186
	v_mov_b32_e32 v154, v133
	v_cvt_pk_fp8_f32 v154, v157, v155
	v_mul_f32_e32 v156, s66, v158
	v_mul_f32_e32 v155, s66, v174
	v_med3_f32 v156, v156, s62, v186
	v_med3_f32 v155, v155, s62, v186
	ds_read_b32 v158, v184 offset:18428
	v_cvt_pk_fp8_f32 v154, v156, v155 op_sel:[0,0,1]
	v_mul_f32_e32 v155, s66, v160
	v_mul_f32_e32 v156, s66, v172
	v_med3_f32 v159, v155, s62, v186
	v_med3_f32 v156, v156, s62, v186
	v_mov_b32_e32 v155, v133
	v_cvt_pk_fp8_f32 v155, v159, v156
	v_mul_f32_e32 v157, s66, v178
	s_waitcnt lgkmcnt(0)
	v_mul_f32_e32 v156, s66, v158
	v_med3_f32 v157, v157, s62, v186
	v_med3_f32 v156, v156, s62, v186
	v_cvt_pk_fp8_f32 v155, v157, v156 op_sel:[0,0,1]
	v_mad_u64_u32 v[192:193], s[18:19], s65, v148, v[176:177]
	v_mad_u64_u32 v[156:157], s[18:19], s65, v150, v[176:177]
	v_lshl_add_u64 v[192:193], v[192:193], 0, v[136:137]
	v_lshl_add_u64 v[156:157], v[156:157], 0, v[136:137]
	global_store_dwordx2 v[192:193], v[190:191], off nt
	global_store_dwordx2 v[156:157], v[154:155], off nt
	s_cbranch_execnz .LBB0_258
	s_branch .LBB0_257

.LBB0_446:
	v_add_u32_e32 v188, 0x4000, v183
	v_add_u32_e32 v189, 0x4008, v183
	v_add_u32_e32 v190, 0x4410, v183
	v_add_u32_e32 v191, 0x4418, v183
	v_add_u32_e32 v192, 0x4820, v183
	v_add_u32_e32 v193, 0x4828, v183
	v_add_u32_e32 v198, 0x4c30, v183
	v_add_u32_e32 v199, 0x4c38, v183
	v_add_u32_e32 v200, 0x5040, v183
	v_add_u32_e32 v201, 0x5048, v183
	v_add_u32_e32 v205, 0x5450, v183
	v_add_u32_e32 v206, 0x5458, v183
	v_add_u32_e32 v207, 0x5860, v183
	v_add_u32_e32 v208, 0x5868, v183
	v_add_u32_e32 v209, 0x5c70, v183
	v_add_u32_e32 v210, 0x5c78, v183
	v_add_u32_e32 v211, 0x6080, v183
	v_add_u32_e32 v212, 0x6088, v183
	v_add_u32_e32 v213, 0x6490, v183
	v_add_u32_e32 v214, 0x6498, v183
	v_add_u32_e32 v215, 0x68a0, v183
	v_add_u32_e32 v216, 0x68a8, v183
	v_add_u32_e32 v217, 0x6cb0, v183
	v_add_u32_e32 v218, 0x6cb8, v183
	v_add_u32_e32 v219, 0x70c0, v183
	v_add_u32_e32 v220, 0x70c8, v183
	v_add_u32_e32 v221, 0x74d0, v183
	v_add_u32_e32 v222, 0x74d8, v183
	v_add_u32_e32 v223, 0x78e0, v183
	v_add_u32_e32 v224, 0x78e8, v183
	v_add_u32_e32 v225, 0x7cf0, v183
	v_add_u32_e32 v226, 0x7cf8, v183
	s_waitcnt vmcnt(31)
	ds_write2_b32 v188, v2, v3 offset1:1
	ds_write2_b32 v189, v4, v5 offset1:1
	s_waitcnt vmcnt(30)
	ds_write2_b32 v190, v6, v7 offset1:1
	ds_write2_b32 v191, v8, v9 offset1:1
	s_waitcnt vmcnt(29)
	ds_write2_b32 v192, v10, v11 offset1:1
	ds_write2_b32 v193, v12, v13 offset1:1
	s_waitcnt vmcnt(28)
	ds_write2_b32 v198, v14, v15 offset1:1
	ds_write2_b32 v199, v16, v17 offset1:1
	s_waitcnt vmcnt(27)
	ds_write2_b32 v200, v18, v19 offset1:1
	ds_write2_b32 v201, v20, v21 offset1:1
	s_waitcnt vmcnt(26)
	ds_write2_b32 v205, v22, v23 offset1:1
	ds_write2_b32 v206, v24, v25 offset1:1
	s_waitcnt vmcnt(25)
	ds_write2_b32 v207, v26, v27 offset1:1
	ds_write2_b32 v208, v28, v29 offset1:1
	s_waitcnt vmcnt(24)
	ds_write2_b32 v209, v30, v31 offset1:1
	ds_write2_b32 v210, v32, v33 offset1:1
	s_waitcnt vmcnt(23)
	ds_write2_b32 v211, v34, v35 offset1:1
	ds_write2_b32 v212, v36, v37 offset1:1
	s_waitcnt vmcnt(22)
	ds_write2_b32 v213, v38, v39 offset1:1
	ds_write2_b32 v214, v40, v41 offset1:1
	s_waitcnt vmcnt(21)
	ds_write2_b32 v215, v42, v43 offset1:1
	ds_write2_b32 v216, v44, v45 offset1:1
	s_waitcnt vmcnt(20)
	ds_write2_b32 v217, v46, v47 offset1:1
	ds_write2_b32 v218, v48, v49 offset1:1
	s_waitcnt vmcnt(19)
	ds_write2_b32 v219, v50, v51 offset1:1
	ds_write2_b32 v220, v52, v53 offset1:1
	s_waitcnt vmcnt(18)
	ds_write2_b32 v221, v54, v55 offset1:1
	ds_write2_b32 v222, v56, v57 offset1:1
	s_waitcnt vmcnt(17)
	ds_write2_b32 v223, v74, v75 offset1:1
	ds_write2_b32 v224, v76, v77 offset1:1
	s_waitcnt vmcnt(16)
	ds_write2_b32 v225, v78, v79 offset1:1
	ds_write2_b32 v226, v80, v81 offset1:1
	s_waitcnt lgkmcnt(0)
	ds_read_b32 v132, v182 offset:16384
	v_cmp_eq_f32_e64 s[14:15], s33, 0
	s_and_b64 vcc, exec, s[14:15]
	v_add_u32_e32 v186, 0x4000, v182
	v_add_u32_e32 v187, 0x4200, v182
	v_add_u32_e32 v185, 0x4400, v182
	s_cbranch_vccnz .LBB0_467
	ds_read2_b32 v[154:155], v186 offset0:56 offset1:65
	ds_read2_b32 v[156:157], v186 offset0:121 offset1:130
	ds_read2_b32 v[158:159], v186 offset0:186 offset1:195
	s_waitcnt lgkmcnt(3)
	v_mul_f32_e32 v160, s33, v132
	v_med3_f32 v160, v160, s56, v184
	s_waitcnt lgkmcnt(2)
	v_mul_f32_e32 v155, s33, v155
	v_med3_f32 v155, v155, s56, v184
	v_mov_b32_e32 v228, v133
	v_cvt_pk_fp8_f32 v228, v160, v155
	ds_read2_b32 v[174:175], v187 offset0:123 offset1:132
	ds_read2_b32 v[160:161], v185 offset0:60 offset1:69
	ds_read2_b32 v[172:173], v185 offset0:125 offset1:134
	s_waitcnt lgkmcnt(4)
	v_mul_f32_e32 v157, s33, v157
	s_waitcnt lgkmcnt(3)
	v_mul_f32_e32 v159, s33, v159
	v_med3_f32 v157, v157, s56, v184
	v_med3_f32 v155, v159, s56, v184
	ds_read2_b32 v[178:179], v185 offset0:190 offset1:199
	v_cvt_pk_fp8_f32 v228, v157, v155 op_sel:[0,0,1]
	s_waitcnt lgkmcnt(3)
	v_mul_f32_e32 v155, s33, v175
	s_waitcnt lgkmcnt(2)
	v_mul_f32_e32 v157, s33, v161
	v_med3_f32 v155, v155, s56, v184
	v_med3_f32 v157, v157, s56, v184
	v_mov_b32_e32 v229, v133
	v_cvt_pk_fp8_f32 v229, v155, v157
	s_waitcnt lgkmcnt(1)
	v_mul_f32_e32 v159, s33, v173
	s_waitcnt lgkmcnt(0)
	v_mul_f32_e32 v155, s33, v179
	v_med3_f32 v157, v159, s56, v184
	v_med3_f32 v155, v155, s56, v184
	v_cvt_pk_fp8_f32 v229, v157, v155 op_sel:[0,0,1]
	ds_read2_b32 v[232:233], v186 offset0:8 offset1:16
	ds_read2_b32 v[234:235], v186 offset0:73 offset1:81
	ds_read2_b32 v[236:237], v186 offset0:138 offset1:146
	ds_read2_b32 v[238:239], v186 offset0:203 offset1:211
	v_mov_b64_e32 v[176:177], s[8:9]
	v_mad_u64_u32 v[230:231], s[14:15], s22, v134, v[176:177]
	v_lshl_add_u64 v[230:231], v[230:231], 0, v[136:137]
	s_waitcnt lgkmcnt(3)
	v_mul_f32_e32 v155, s33, v232
	s_waitcnt lgkmcnt(2)
	v_mul_f32_e32 v157, s33, v234
	global_store_dwordx2 v[230:231], v[228:229], off nt
	v_med3_f32 v155, v155, s56, v184
	v_med3_f32 v157, v157, s56, v184
	v_mov_b32_e32 v228, v133
	v_cvt_pk_fp8_f32 v228, v155, v157
	ds_read2_b32 v[230:231], v185 offset0:12 offset1:20
	ds_read2_b32 v[240:241], v185 offset0:77 offset1:85
	ds_read2_b32 v[242:243], v185 offset0:142 offset1:150
	s_waitcnt lgkmcnt(4)
	v_mul_f32_e32 v159, s33, v236
	s_waitcnt lgkmcnt(3)
	v_mul_f32_e32 v161, s33, v238
	v_med3_f32 v159, v159, s56, v184
	v_med3_f32 v155, v161, s56, v184
	ds_read2_b32 v[244:245], v185 offset0:207 offset1:215
	v_cvt_pk_fp8_f32 v228, v159, v155 op_sel:[0,0,1]
	s_waitcnt lgkmcnt(3)
	v_mul_f32_e32 v155, s33, v230
	s_waitcnt lgkmcnt(2)
	v_mul_f32_e32 v157, s33, v240
	v_med3_f32 v155, v155, s56, v184
	v_med3_f32 v157, v157, s56, v184
	v_mov_b32_e32 v229, v133
	v_cvt_pk_fp8_f32 v229, v155, v157
	s_waitcnt lgkmcnt(1)
	v_mul_f32_e32 v159, s33, v242
	s_waitcnt lgkmcnt(0)
	v_mul_f32_e32 v155, s33, v244
	v_med3_f32 v157, v159, s56, v184
	v_med3_f32 v155, v155, s56, v184
	v_cvt_pk_fp8_f32 v229, v157, v155 op_sel:[0,0,1]
	v_mad_u64_u32 v[246:247], s[14:15], s22, v138, v[176:177]
	v_lshl_add_u64 v[246:247], v[246:247], 0, v[136:137]
	v_mul_f32_e32 v155, s33, v233
	v_mul_f32_e32 v157, s33, v235
	global_store_dwordx2 v[246:247], v[228:229], off nt
	v_med3_f32 v155, v155, s56, v184
	v_med3_f32 v157, v157, s56, v184
	v_mov_b32_e32 v228, v133
	v_cvt_pk_fp8_f32 v228, v155, v157
	v_mul_f32_e32 v159, s33, v237
	v_mul_f32_e32 v155, s33, v239
	v_med3_f32 v157, v159, s56, v184
	v_med3_f32 v155, v155, s56, v184
	v_cvt_pk_fp8_f32 v228, v157, v155 op_sel:[0,0,1]
	v_mul_f32_e32 v155, s33, v231
	v_mul_f32_e32 v157, s33, v241
	v_med3_f32 v155, v155, s56, v184
	v_med3_f32 v157, v157, s56, v184
	v_mov_b32_e32 v229, v133
	v_cvt_pk_fp8_f32 v229, v155, v157
	v_mul_f32_e32 v159, s33, v243
	v_mul_f32_e32 v155, s33, v245
	v_med3_f32 v157, v159, s56, v184
	v_med3_f32 v155, v155, s56, v184
	v_cvt_pk_fp8_f32 v229, v157, v155 op_sel:[0,0,1]
	ds_read2_b32 v[232:233], v186 offset0:24 offset1:32
	ds_read2_b32 v[234:235], v186 offset0:89 offset1:97
	ds_read2_b32 v[236:237], v186 offset0:154 offset1:162
	ds_read2_b32 v[238:239], v186 offset0:219 offset1:227
	v_mad_u64_u32 v[230:231], s[14:15], s22, v140, v[176:177]
	v_lshl_add_u64 v[230:231], v[230:231], 0, v[136:137]
	s_waitcnt lgkmcnt(3)
	v_mul_f32_e32 v155, s33, v232
	s_waitcnt lgkmcnt(2)
	v_mul_f32_e32 v157, s33, v234
	global_store_dwordx2 v[230:231], v[228:229], off nt
	v_med3_f32 v155, v155, s56, v184
	v_med3_f32 v157, v157, s56, v184
	v_mov_b32_e32 v228, v133
	v_cvt_pk_fp8_f32 v228, v155, v157
	ds_read2_b32 v[230:231], v185 offset0:28 offset1:36
	ds_read2_b32 v[240:241], v185 offset0:93 offset1:101
	ds_read2_b32 v[242:243], v185 offset0:158 offset1:166
	s_waitcnt lgkmcnt(4)
	v_mul_f32_e32 v159, s33, v236
	s_waitcnt lgkmcnt(3)
	v_mul_f32_e32 v161, s33, v238
	v_med3_f32 v159, v159, s56, v184
	v_med3_f32 v155, v161, s56, v184
	ds_read2_b32 v[244:245], v185 offset0:223 offset1:231
	v_cvt_pk_fp8_f32 v228, v159, v155 op_sel:[0,0,1]
	s_waitcnt lgkmcnt(3)
	v_mul_f32_e32 v155, s33, v230
	s_waitcnt lgkmcnt(2)
	v_mul_f32_e32 v157, s33, v240
	v_med3_f32 v155, v155, s56, v184
	v_med3_f32 v157, v157, s56, v184
	v_mov_b32_e32 v229, v133
	v_cvt_pk_fp8_f32 v229, v155, v157
	s_waitcnt lgkmcnt(1)
	v_mul_f32_e32 v159, s33, v242
	s_waitcnt lgkmcnt(0)
	v_mul_f32_e32 v155, s33, v244
	v_med3_f32 v157, v159, s56, v184
	v_med3_f32 v155, v155, s56, v184
	v_cvt_pk_fp8_f32 v229, v157, v155 op_sel:[0,0,1]
	v_mad_u64_u32 v[246:247], s[14:15], s22, v142, v[176:177]
	v_lshl_add_u64 v[246:247], v[246:247], 0, v[136:137]
	v_mul_f32_e32 v155, s33, v233
	v_mul_f32_e32 v157, s33, v235
	global_store_dwordx2 v[246:247], v[228:229], off nt
	v_med3_f32 v155, v155, s56, v184
	v_med3_f32 v157, v157, s56, v184
	v_mov_b32_e32 v228, v133
	v_cvt_pk_fp8_f32 v228, v155, v157
	v_mul_f32_e32 v159, s33, v237
	v_mul_f32_e32 v155, s33, v239
	v_med3_f32 v157, v159, s56, v184
	v_med3_f32 v155, v155, s56, v184
	v_cvt_pk_fp8_f32 v228, v157, v155 op_sel:[0,0,1]
	v_mul_f32_e32 v155, s33, v231
	v_mul_f32_e32 v157, s33, v241
	v_med3_f32 v155, v155, s56, v184
	v_med3_f32 v157, v157, s56, v184
	v_mov_b32_e32 v229, v133
	v_cvt_pk_fp8_f32 v229, v155, v157
	v_mul_f32_e32 v159, s33, v243
	v_mul_f32_e32 v155, s33, v245
	v_med3_f32 v157, v159, s56, v184
	v_med3_f32 v155, v155, s56, v184
	v_cvt_pk_fp8_f32 v229, v157, v155 op_sel:[0,0,1]
	ds_read2_b32 v[232:233], v186 offset0:40 offset1:48
	ds_read2_b32 v[234:235], v186 offset0:105 offset1:113
	ds_read2_b32 v[236:237], v186 offset0:170 offset1:178
	ds_read2_b32 v[238:239], v186 offset0:235 offset1:243
	v_mad_u64_u32 v[230:231], s[14:15], s22, v144, v[176:177]
	v_lshl_add_u64 v[230:231], v[230:231], 0, v[136:137]
	s_waitcnt lgkmcnt(3)
	v_mul_f32_e32 v155, s33, v232
	s_waitcnt lgkmcnt(2)
	v_mul_f32_e32 v157, s33, v234
	global_store_dwordx2 v[230:231], v[228:229], off nt
	v_med3_f32 v155, v155, s56, v184
	v_med3_f32 v157, v157, s56, v184
	v_mov_b32_e32 v228, v133
	v_cvt_pk_fp8_f32 v228, v155, v157
	ds_read2_b32 v[230:231], v185 offset0:44 offset1:52
	ds_read2_b32 v[240:241], v185 offset0:109 offset1:117
	ds_read2_b32 v[242:243], v185 offset0:174 offset1:182
	s_waitcnt lgkmcnt(4)
	v_mul_f32_e32 v159, s33, v236
	s_waitcnt lgkmcnt(3)
	v_mul_f32_e32 v161, s33, v238
	v_med3_f32 v159, v159, s56, v184
	v_med3_f32 v155, v161, s56, v184
	ds_read2_b32 v[244:245], v185 offset0:239 offset1:247
	v_cvt_pk_fp8_f32 v228, v159, v155 op_sel:[0,0,1]
	s_waitcnt lgkmcnt(3)
	v_mul_f32_e32 v155, s33, v230
	s_waitcnt lgkmcnt(2)
	v_mul_f32_e32 v157, s33, v240
	v_med3_f32 v155, v155, s56, v184
	v_med3_f32 v157, v157, s56, v184
	v_mov_b32_e32 v229, v133
	v_cvt_pk_fp8_f32 v229, v155, v157
	s_waitcnt lgkmcnt(1)
	v_mul_f32_e32 v159, s33, v242
	s_waitcnt lgkmcnt(0)
	v_mul_f32_e32 v155, s33, v244
	v_med3_f32 v157, v159, s56, v184
	v_med3_f32 v155, v155, s56, v184
	v_cvt_pk_fp8_f32 v229, v157, v155 op_sel:[0,0,1]
	v_mad_u64_u32 v[246:247], s[14:15], s22, v146, v[176:177]
	v_lshl_add_u64 v[246:247], v[246:247], 0, v[136:137]
	v_mul_f32_e32 v155, s33, v233
	v_mul_f32_e32 v157, s33, v235
	global_store_dwordx2 v[246:247], v[228:229], off nt
	v_med3_f32 v155, v155, s56, v184
	v_med3_f32 v157, v157, s56, v184
	v_mov_b32_e32 v228, v133
	v_cvt_pk_fp8_f32 v228, v155, v157
	v_mul_f32_e32 v159, s33, v237
	v_mul_f32_e32 v155, s33, v239
	v_med3_f32 v157, v159, s56, v184
	v_med3_f32 v155, v155, s56, v184
	v_cvt_pk_fp8_f32 v228, v157, v155 op_sel:[0,0,1]
	v_mul_f32_e32 v155, s33, v231
	v_mul_f32_e32 v157, s33, v241
	v_med3_f32 v155, v155, s56, v184
	v_med3_f32 v157, v157, s56, v184
	v_mov_b32_e32 v229, v133
	v_cvt_pk_fp8_f32 v229, v155, v157
	v_mul_f32_e32 v159, s33, v243
	v_mul_f32_e32 v155, s33, v245
	v_med3_f32 v157, v159, s56, v184
	v_med3_f32 v155, v155, s56, v184
	v_cvt_pk_fp8_f32 v229, v157, v155 op_sel:[0,0,1]
	v_mul_f32_e32 v154, s33, v154
	v_mul_f32_e32 v155, s33, v156
	v_med3_f32 v157, v154, s56, v184
	v_med3_f32 v155, v155, s56, v184
	v_mov_b32_e32 v154, v133
	v_cvt_pk_fp8_f32 v154, v157, v155
	v_mul_f32_e32 v156, s33, v158
	v_mul_f32_e32 v155, s33, v174
	v_med3_f32 v156, v156, s56, v184
	v_med3_f32 v155, v155, s56, v184
	ds_read_b32 v158, v182 offset:18428
	v_cvt_pk_fp8_f32 v154, v156, v155 op_sel:[0,0,1]
	v_mul_f32_e32 v155, s33, v160
	v_mul_f32_e32 v156, s33, v172
	v_med3_f32 v159, v155, s56, v184
	v_med3_f32 v156, v156, s56, v184
	v_mov_b32_e32 v155, v133
	v_cvt_pk_fp8_f32 v155, v159, v156
	v_mul_f32_e32 v157, s33, v178
	s_waitcnt lgkmcnt(0)
	v_mul_f32_e32 v156, s33, v158
	v_med3_f32 v157, v157, s56, v184
	v_med3_f32 v156, v156, s56, v184
	v_cvt_pk_fp8_f32 v155, v157, v156 op_sel:[0,0,1]
	v_mad_u64_u32 v[230:231], s[14:15], s22, v148, v[176:177]
	v_mad_u64_u32 v[156:157], s[14:15], s22, v150, v[176:177]
	v_lshl_add_u64 v[230:231], v[230:231], 0, v[136:137]
	v_lshl_add_u64 v[156:157], v[156:157], 0, v[136:137]
	global_store_dwordx2 v[230:231], v[228:229], off nt
	global_store_dwordx2 v[156:157], v[154:155], off nt
	s_cbranch_execnz .LBB0_449

.LBB0_483:
	s_waitcnt vmcnt(31)
	ds_write2_b32 v188, v62, v63 offset1:1
	ds_write2_b32 v189, v64, v65 offset1:1
	s_waitcnt vmcnt(30)
	ds_write2_b32 v190, v58, v59 offset1:1
	ds_write2_b32 v191, v60, v61 offset1:1
	s_waitcnt vmcnt(29)
	ds_write2_b32 v192, v70, v71 offset1:1
	ds_write2_b32 v193, v72, v73 offset1:1
	s_waitcnt vmcnt(28)
	ds_write2_b32 v198, v66, v67 offset1:1
	ds_write2_b32 v199, v68, v69 offset1:1
	s_waitcnt vmcnt(27)
	ds_write2_b32 v200, v86, v87 offset1:1
	ds_write2_b32 v201, v88, v89 offset1:1
	s_waitcnt vmcnt(26)
	ds_write2_b32 v205, v82, v83 offset1:1
	ds_write2_b32 v206, v84, v85 offset1:1
	s_waitcnt vmcnt(25)
	ds_write2_b32 v207, v94, v95 offset1:1
	ds_write2_b32 v208, v96, v97 offset1:1
	s_waitcnt vmcnt(24)
	ds_write2_b32 v209, v90, v91 offset1:1
	ds_write2_b32 v210, v92, v93 offset1:1
	s_waitcnt vmcnt(23)
	ds_write2_b32 v211, v102, v103 offset1:1
	ds_write2_b32 v212, v104, v105 offset1:1
	s_waitcnt vmcnt(22)
	ds_write2_b32 v213, v98, v99 offset1:1
	ds_write2_b32 v214, v100, v101 offset1:1
	s_waitcnt vmcnt(21)
	ds_write2_b32 v215, v110, v111 offset1:1
	ds_write2_b32 v216, v112, v113 offset1:1
	s_waitcnt vmcnt(20)
	ds_write2_b32 v217, v106, v107 offset1:1
	ds_write2_b32 v218, v108, v109 offset1:1
	s_waitcnt vmcnt(19)
	ds_write2_b32 v219, v118, v119 offset1:1
	ds_write2_b32 v220, v120, v121 offset1:1
	s_waitcnt vmcnt(18)
	ds_write2_b32 v221, v114, v115 offset1:1
	ds_write2_b32 v222, v116, v117 offset1:1
	s_waitcnt vmcnt(17)
	ds_write2_b32 v223, v126, v127 offset1:1
	ds_write2_b32 v224, v128, v129 offset1:1
	s_waitcnt vmcnt(16)
	ds_write2_b32 v225, v122, v123 offset1:1
	ds_write2_b32 v226, v124, v125 offset1:1
	s_waitcnt lgkmcnt(0)
	s_waitcnt lgkmcnt(14)
	ds_read_b32 v132, v182 offset:16384
	v_cmp_eq_f32_e64 s[12:13], s60, 0
	s_and_b64 vcc, exec, s[12:13]
	s_cbranch_vccnz .LBB0_485
	ds_read2_b32 v[154:155], v186 offset0:56 offset1:65
	ds_read2_b32 v[156:157], v186 offset0:121 offset1:130
	ds_read2_b32 v[158:159], v186 offset0:186 offset1:195
	s_waitcnt lgkmcnt(3)
	v_mul_f32_e32 v160, s60, v132
	v_med3_f32 v160, v160, s56, v184
	s_waitcnt lgkmcnt(2)
	v_mul_f32_e32 v155, s60, v155
	v_med3_f32 v155, v155, s56, v184
	v_mov_b32_e32 v188, v133
	v_cvt_pk_fp8_f32 v188, v160, v155
	ds_read2_b32 v[174:175], v187 offset0:123 offset1:132
	ds_read2_b32 v[160:161], v185 offset0:60 offset1:69
	ds_read2_b32 v[172:173], v185 offset0:125 offset1:134
	s_waitcnt lgkmcnt(4)
	v_mul_f32_e32 v157, s60, v157
	s_waitcnt lgkmcnt(3)
	v_mul_f32_e32 v159, s60, v159
	v_med3_f32 v157, v157, s56, v184
	v_med3_f32 v155, v159, s56, v184
	ds_read2_b32 v[178:179], v185 offset0:190 offset1:199
	v_cvt_pk_fp8_f32 v188, v157, v155 op_sel:[0,0,1]
	s_waitcnt lgkmcnt(3)
	v_mul_f32_e32 v155, s60, v175
	s_waitcnt lgkmcnt(2)
	v_mul_f32_e32 v157, s60, v161
	v_med3_f32 v155, v155, s56, v184
	v_med3_f32 v157, v157, s56, v184
	v_mov_b32_e32 v189, v133
	v_cvt_pk_fp8_f32 v189, v155, v157
	s_waitcnt lgkmcnt(1)
	v_mul_f32_e32 v159, s60, v173
	s_waitcnt lgkmcnt(0)
	v_mul_f32_e32 v155, s60, v179
	v_med3_f32 v157, v159, s56, v184
	v_med3_f32 v155, v155, s56, v184
	v_cvt_pk_fp8_f32 v189, v157, v155 op_sel:[0,0,1]
	ds_read2_b32 v[192:193], v186 offset0:8 offset1:16
	ds_read2_b32 v[198:199], v186 offset0:73 offset1:81
	ds_read2_b32 v[200:201], v186 offset0:138 offset1:146
	ds_read2_b32 v[206:207], v186 offset0:203 offset1:211
	v_mov_b64_e32 v[176:177], s[10:11]
	v_mad_u64_u32 v[190:191], s[12:13], s59, v134, v[176:177]
	v_lshl_add_u64 v[190:191], v[190:191], 0, v[136:137]
	s_waitcnt lgkmcnt(3)
	v_mul_f32_e32 v155, s60, v192
	s_waitcnt lgkmcnt(2)
	v_mul_f32_e32 v157, s60, v198
	global_store_dwordx2 v[190:191], v[188:189], off nt
	v_med3_f32 v155, v155, s56, v184
	v_med3_f32 v157, v157, s56, v184
	v_mov_b32_e32 v188, v133
	v_cvt_pk_fp8_f32 v188, v155, v157
	ds_read2_b32 v[190:191], v185 offset0:12 offset1:20
	ds_read2_b32 v[208:209], v185 offset0:77 offset1:85
	ds_read2_b32 v[210:211], v185 offset0:142 offset1:150
	s_waitcnt lgkmcnt(4)
	v_mul_f32_e32 v159, s60, v200
	s_waitcnt lgkmcnt(3)
	v_mul_f32_e32 v161, s60, v206
	v_med3_f32 v159, v159, s56, v184
	v_med3_f32 v155, v161, s56, v184
	ds_read2_b32 v[212:213], v185 offset0:207 offset1:215
	v_cvt_pk_fp8_f32 v188, v159, v155 op_sel:[0,0,1]
	s_waitcnt lgkmcnt(3)
	v_mul_f32_e32 v155, s60, v190
	s_waitcnt lgkmcnt(2)
	v_mul_f32_e32 v157, s60, v208
	v_med3_f32 v155, v155, s56, v184
	v_med3_f32 v157, v157, s56, v184
	v_mov_b32_e32 v189, v133
	v_cvt_pk_fp8_f32 v189, v155, v157
	s_waitcnt lgkmcnt(1)
	v_mul_f32_e32 v159, s60, v210
	s_waitcnt lgkmcnt(0)
	v_mul_f32_e32 v155, s60, v212
	v_med3_f32 v157, v159, s56, v184
	v_med3_f32 v155, v155, s56, v184
	v_cvt_pk_fp8_f32 v189, v157, v155 op_sel:[0,0,1]
	v_mad_u64_u32 v[214:215], s[12:13], s59, v138, v[176:177]
	v_lshl_add_u64 v[214:215], v[214:215], 0, v[136:137]
	v_mul_f32_e32 v155, s60, v193
	v_mul_f32_e32 v157, s60, v199
	global_store_dwordx2 v[214:215], v[188:189], off nt
	v_med3_f32 v155, v155, s56, v184
	v_med3_f32 v157, v157, s56, v184
	v_mov_b32_e32 v188, v133
	v_cvt_pk_fp8_f32 v188, v155, v157
	v_mul_f32_e32 v159, s60, v201
	v_mul_f32_e32 v155, s60, v207
	v_med3_f32 v157, v159, s56, v184
	v_med3_f32 v155, v155, s56, v184
	v_cvt_pk_fp8_f32 v188, v157, v155 op_sel:[0,0,1]
	v_mul_f32_e32 v155, s60, v191
	v_mul_f32_e32 v157, s60, v209
	v_med3_f32 v155, v155, s56, v184
	v_med3_f32 v157, v157, s56, v184
	v_mov_b32_e32 v189, v133
	v_cvt_pk_fp8_f32 v189, v155, v157
	v_mul_f32_e32 v159, s60, v211
	v_mul_f32_e32 v155, s60, v213
	v_med3_f32 v157, v159, s56, v184
	v_med3_f32 v155, v155, s56, v184
	v_cvt_pk_fp8_f32 v189, v157, v155 op_sel:[0,0,1]
	ds_read2_b32 v[192:193], v186 offset0:24 offset1:32
	ds_read2_b32 v[198:199], v186 offset0:89 offset1:97
	ds_read2_b32 v[200:201], v186 offset0:154 offset1:162
	ds_read2_b32 v[206:207], v186 offset0:219 offset1:227
	v_mad_u64_u32 v[190:191], s[12:13], s59, v140, v[176:177]
	v_lshl_add_u64 v[190:191], v[190:191], 0, v[136:137]
	s_waitcnt lgkmcnt(3)
	v_mul_f32_e32 v155, s60, v192
	s_waitcnt lgkmcnt(2)
	v_mul_f32_e32 v157, s60, v198
	global_store_dwordx2 v[190:191], v[188:189], off nt
	v_med3_f32 v155, v155, s56, v184
	v_med3_f32 v157, v157, s56, v184
	v_mov_b32_e32 v188, v133
	v_cvt_pk_fp8_f32 v188, v155, v157
	ds_read2_b32 v[190:191], v185 offset0:28 offset1:36
	ds_read2_b32 v[208:209], v185 offset0:93 offset1:101
	ds_read2_b32 v[210:211], v185 offset0:158 offset1:166
	s_waitcnt lgkmcnt(4)
	v_mul_f32_e32 v159, s60, v200
	s_waitcnt lgkmcnt(3)
	v_mul_f32_e32 v161, s60, v206
	v_med3_f32 v159, v159, s56, v184
	v_med3_f32 v155, v161, s56, v184
	ds_read2_b32 v[212:213], v185 offset0:223 offset1:231
	v_cvt_pk_fp8_f32 v188, v159, v155 op_sel:[0,0,1]
	s_waitcnt lgkmcnt(3)
	v_mul_f32_e32 v155, s60, v190
	s_waitcnt lgkmcnt(2)
	v_mul_f32_e32 v157, s60, v208
	v_med3_f32 v155, v155, s56, v184
	v_med3_f32 v157, v157, s56, v184
	v_mov_b32_e32 v189, v133
	v_cvt_pk_fp8_f32 v189, v155, v157
	s_waitcnt lgkmcnt(1)
	v_mul_f32_e32 v159, s60, v210
	s_waitcnt lgkmcnt(0)
	v_mul_f32_e32 v155, s60, v212
	v_med3_f32 v157, v159, s56, v184
	v_med3_f32 v155, v155, s56, v184
	v_cvt_pk_fp8_f32 v189, v157, v155 op_sel:[0,0,1]
	v_mad_u64_u32 v[214:215], s[12:13], s59, v142, v[176:177]
	v_lshl_add_u64 v[214:215], v[214:215], 0, v[136:137]
	v_mul_f32_e32 v155, s60, v193
	v_mul_f32_e32 v157, s60, v199
	global_store_dwordx2 v[214:215], v[188:189], off nt
	v_med3_f32 v155, v155, s56, v184
	v_med3_f32 v157, v157, s56, v184
	v_mov_b32_e32 v188, v133
	v_cvt_pk_fp8_f32 v188, v155, v157
	v_mul_f32_e32 v159, s60, v201
	v_mul_f32_e32 v155, s60, v207
	v_med3_f32 v157, v159, s56, v184
	v_med3_f32 v155, v155, s56, v184
	v_cvt_pk_fp8_f32 v188, v157, v155 op_sel:[0,0,1]
	v_mul_f32_e32 v155, s60, v191
	v_mul_f32_e32 v157, s60, v209
	v_med3_f32 v155, v155, s56, v184
	v_med3_f32 v157, v157, s56, v184
	v_mov_b32_e32 v189, v133
	v_cvt_pk_fp8_f32 v189, v155, v157
	v_mul_f32_e32 v159, s60, v211
	v_mul_f32_e32 v155, s60, v213
	v_med3_f32 v157, v159, s56, v184
	v_med3_f32 v155, v155, s56, v184
	v_cvt_pk_fp8_f32 v189, v157, v155 op_sel:[0,0,1]
	ds_read2_b32 v[192:193], v186 offset0:40 offset1:48
	ds_read2_b32 v[198:199], v186 offset0:105 offset1:113
	ds_read2_b32 v[200:201], v186 offset0:170 offset1:178
	ds_read2_b32 v[206:207], v186 offset0:235 offset1:243
	v_mad_u64_u32 v[190:191], s[12:13], s59, v144, v[176:177]
	v_lshl_add_u64 v[190:191], v[190:191], 0, v[136:137]
	s_waitcnt lgkmcnt(3)
	v_mul_f32_e32 v155, s60, v192
	s_waitcnt lgkmcnt(2)
	v_mul_f32_e32 v157, s60, v198
	global_store_dwordx2 v[190:191], v[188:189], off nt
	v_med3_f32 v155, v155, s56, v184
	v_med3_f32 v157, v157, s56, v184
	v_mov_b32_e32 v188, v133
	v_cvt_pk_fp8_f32 v188, v155, v157
	ds_read2_b32 v[190:191], v185 offset0:44 offset1:52
	ds_read2_b32 v[208:209], v185 offset0:109 offset1:117
	ds_read2_b32 v[210:211], v185 offset0:174 offset1:182
	s_waitcnt lgkmcnt(4)
	v_mul_f32_e32 v159, s60, v200
	s_waitcnt lgkmcnt(3)
	v_mul_f32_e32 v161, s60, v206
	v_med3_f32 v159, v159, s56, v184
	v_med3_f32 v155, v161, s56, v184
	ds_read2_b32 v[212:213], v185 offset0:239 offset1:247
	v_cvt_pk_fp8_f32 v188, v159, v155 op_sel:[0,0,1]
	s_waitcnt lgkmcnt(3)
	v_mul_f32_e32 v155, s60, v190
	s_waitcnt lgkmcnt(2)
	v_mul_f32_e32 v157, s60, v208
	v_med3_f32 v155, v155, s56, v184
	v_med3_f32 v157, v157, s56, v184
	v_mov_b32_e32 v189, v133
	v_cvt_pk_fp8_f32 v189, v155, v157
	s_waitcnt lgkmcnt(1)
	v_mul_f32_e32 v159, s60, v210
	s_waitcnt lgkmcnt(0)
	v_mul_f32_e32 v155, s60, v212
	v_med3_f32 v157, v159, s56, v184
	v_med3_f32 v155, v155, s56, v184
	v_cvt_pk_fp8_f32 v189, v157, v155 op_sel:[0,0,1]
	v_mad_u64_u32 v[214:215], s[12:13], s59, v146, v[176:177]
	v_lshl_add_u64 v[214:215], v[214:215], 0, v[136:137]
	v_mul_f32_e32 v155, s60, v193
	v_mul_f32_e32 v157, s60, v199
	global_store_dwordx2 v[214:215], v[188:189], off nt
	v_med3_f32 v155, v155, s56, v184
	v_med3_f32 v157, v157, s56, v184
	v_mov_b32_e32 v188, v133
	v_cvt_pk_fp8_f32 v188, v155, v157
	v_mul_f32_e32 v159, s60, v201
	v_mul_f32_e32 v155, s60, v207
	v_med3_f32 v157, v159, s56, v184
	v_med3_f32 v155, v155, s56, v184
	v_cvt_pk_fp8_f32 v188, v157, v155 op_sel:[0,0,1]
	v_mul_f32_e32 v155, s60, v191
	v_mul_f32_e32 v157, s60, v209
	v_med3_f32 v155, v155, s56, v184
	v_med3_f32 v157, v157, s56, v184
	v_mov_b32_e32 v189, v133
	v_cvt_pk_fp8_f32 v189, v155, v157
	v_mul_f32_e32 v159, s60, v211
	v_mul_f32_e32 v155, s60, v213
	v_med3_f32 v157, v159, s56, v184
	v_med3_f32 v155, v155, s56, v184
	v_cvt_pk_fp8_f32 v189, v157, v155 op_sel:[0,0,1]
	v_mul_f32_e32 v154, s60, v154
	v_mul_f32_e32 v155, s60, v156
	v_med3_f32 v157, v154, s56, v184
	v_med3_f32 v155, v155, s56, v184
	v_mov_b32_e32 v154, v133
	v_cvt_pk_fp8_f32 v154, v157, v155
	v_mul_f32_e32 v156, s60, v158
	v_mul_f32_e32 v155, s60, v174
	v_med3_f32 v156, v156, s56, v184
	v_med3_f32 v155, v155, s56, v184
	ds_read_b32 v158, v182 offset:18428
	v_cvt_pk_fp8_f32 v154, v156, v155 op_sel:[0,0,1]
	v_mul_f32_e32 v155, s60, v160
	v_mul_f32_e32 v156, s60, v172
	v_med3_f32 v159, v155, s56, v184
	v_med3_f32 v156, v156, s56, v184
	v_mov_b32_e32 v155, v133
	v_cvt_pk_fp8_f32 v155, v159, v156
	v_mul_f32_e32 v157, s60, v178
	s_waitcnt lgkmcnt(0)
	v_mul_f32_e32 v156, s60, v158
	v_med3_f32 v157, v157, s56, v184
	v_med3_f32 v156, v156, s56, v184
	v_cvt_pk_fp8_f32 v155, v157, v156 op_sel:[0,0,1]
	v_mad_u64_u32 v[190:191], s[12:13], s59, v148, v[176:177]
	v_mad_u64_u32 v[156:157], s[12:13], s59, v150, v[176:177]
	v_lshl_add_u64 v[190:191], v[190:191], 0, v[136:137]
	v_lshl_add_u64 v[156:157], v[156:157], 0, v[136:137]
	global_store_dwordx2 v[190:191], v[188:189], off nt
	global_store_dwordx2 v[156:157], v[154:155], off nt
	s_cbranch_execnz .LBB0_415
	s_branch .LBB0_414

.LBB0_1732:
	v_add_u32_e32 v183, 0x4000, v178
	v_add_u32_e32 v184, 0x4008, v178
	v_add_u32_e32 v185, 0x4410, v178
	v_add_u32_e32 v186, 0x4418, v178
	v_add_u32_e32 v187, 0x4820, v178
	v_add_u32_e32 v188, 0x4828, v178
	v_add_u32_e32 v189, 0x4c30, v178
	v_add_u32_e32 v190, 0x4c38, v178
	v_add_u32_e32 v191, 0x5040, v178
	v_add_u32_e32 v192, 0x5048, v178
	v_add_u32_e32 v193, 0x5450, v178
	v_add_u32_e32 v195, 0x5458, v178
	v_add_u32_e32 v199, 0x5860, v178
	v_add_u32_e32 v201, 0x5868, v178
	v_add_u32_e32 v202, 0x5c70, v178
	v_add_u32_e32 v203, 0x5c78, v178
	v_add_u32_e32 v204, 0x6080, v178
	v_add_u32_e32 v205, 0x6088, v178
	v_add_u32_e32 v206, 0x6490, v178
	v_add_u32_e32 v207, 0x6498, v178
	v_add_u32_e32 v208, 0x68a0, v178
	v_add_u32_e32 v209, 0x68a8, v178
	v_add_u32_e32 v210, 0x6cb0, v178
	v_add_u32_e32 v211, 0x6cb8, v178
	v_add_u32_e32 v212, 0x70c0, v178
	v_add_u32_e32 v213, 0x70c8, v178
	v_add_u32_e32 v214, 0x74d0, v178
	v_add_u32_e32 v215, 0x74d8, v178
	v_add_u32_e32 v216, 0x78e0, v178
	v_add_u32_e32 v217, 0x78e8, v178
	v_add_u32_e32 v218, 0x7cf0, v178
	v_add_u32_e32 v219, 0x7cf8, v178
	s_waitcnt vmcnt(31)
	ds_write2_b32 v183, v2, v3 offset1:1
	ds_write2_b32 v184, v4, v5 offset1:1
	s_waitcnt vmcnt(30)
	ds_write2_b32 v185, v6, v7 offset1:1
	ds_write2_b32 v186, v8, v9 offset1:1
	s_waitcnt vmcnt(29)
	ds_write2_b32 v187, v10, v11 offset1:1
	ds_write2_b32 v188, v12, v13 offset1:1
	s_waitcnt vmcnt(28)
	ds_write2_b32 v189, v14, v15 offset1:1
	ds_write2_b32 v190, v16, v17 offset1:1
	s_waitcnt vmcnt(27)
	ds_write2_b32 v191, v18, v19 offset1:1
	ds_write2_b32 v192, v20, v21 offset1:1
	s_waitcnt vmcnt(26)
	ds_write2_b32 v193, v22, v23 offset1:1
	ds_write2_b32 v195, v24, v25 offset1:1
	s_waitcnt vmcnt(25)
	ds_write2_b32 v199, v26, v27 offset1:1
	ds_write2_b32 v201, v28, v29 offset1:1
	s_waitcnt vmcnt(24)
	ds_write2_b32 v202, v30, v31 offset1:1
	ds_write2_b32 v203, v32, v33 offset1:1
	s_waitcnt vmcnt(23)
	ds_write2_b32 v204, v34, v35 offset1:1
	ds_write2_b32 v205, v36, v37 offset1:1
	s_waitcnt vmcnt(22)
	ds_write2_b32 v206, v38, v39 offset1:1
	ds_write2_b32 v207, v40, v41 offset1:1
	s_waitcnt vmcnt(21)
	ds_write2_b32 v208, v42, v43 offset1:1
	ds_write2_b32 v209, v44, v45 offset1:1
	s_waitcnt vmcnt(20)
	ds_write2_b32 v210, v46, v47 offset1:1
	ds_write2_b32 v211, v48, v49 offset1:1
	s_waitcnt vmcnt(19)
	ds_write2_b32 v212, v50, v51 offset1:1
	ds_write2_b32 v213, v52, v53 offset1:1
	s_waitcnt vmcnt(18)
	ds_write2_b32 v214, v54, v55 offset1:1
	ds_write2_b32 v215, v56, v57 offset1:1
	s_waitcnt vmcnt(17)
	ds_write2_b32 v216, v66, v67 offset1:1
	ds_write2_b32 v217, v68, v69 offset1:1
	s_waitcnt vmcnt(16)
	ds_write2_b32 v218, v70, v71 offset1:1
	ds_write2_b32 v219, v72, v73 offset1:1
	s_waitcnt lgkmcnt(0)
	ds_read_b32 v132, v177 offset:16384
	v_cmp_eq_f32_e64 s[6:7], s55, 0
	s_and_b64 vcc, exec, s[6:7]
	v_add_u32_e32 v181, 0x4000, v177
	v_add_u32_e32 v182, 0x4200, v177
	v_add_u32_e32 v180, 0x4400, v177
	s_cbranch_vccnz .LBB0_1753
	ds_read2_b32 v[154:155], v181 offset0:56 offset1:65
	ds_read2_b32 v[156:157], v181 offset0:121 offset1:130
	ds_read2_b32 v[158:159], v181 offset0:186 offset1:195
	s_waitcnt lgkmcnt(3)
	v_mul_f32_e32 v160, s55, v132
	v_med3_f32 v160, v160, s47, v179
	s_waitcnt lgkmcnt(2)
	v_mul_f32_e32 v155, s55, v155
	v_med3_f32 v155, v155, s47, v179
	v_mov_b32_e32 v220, v133
	v_cvt_pk_fp8_f32 v220, v160, v155
	ds_read2_b32 v[164:165], v182 offset0:123 offset1:132
	ds_read2_b32 v[160:161], v180 offset0:60 offset1:69
	ds_read2_b32 v[162:163], v180 offset0:125 offset1:134
	s_waitcnt lgkmcnt(4)
	v_mul_f32_e32 v157, s55, v157
	s_waitcnt lgkmcnt(3)
	v_mul_f32_e32 v159, s55, v159
	v_med3_f32 v157, v157, s47, v179
	v_med3_f32 v155, v159, s47, v179
	ds_read2_b32 v[168:169], v180 offset0:190 offset1:199
	v_cvt_pk_fp8_f32 v220, v157, v155 op_sel:[0,0,1]
	s_waitcnt lgkmcnt(3)
	v_mul_f32_e32 v155, s55, v165
	s_waitcnt lgkmcnt(2)
	v_mul_f32_e32 v157, s55, v161
	v_med3_f32 v155, v155, s47, v179
	v_med3_f32 v157, v157, s47, v179
	v_mov_b32_e32 v221, v133
	v_cvt_pk_fp8_f32 v221, v155, v157
	s_waitcnt lgkmcnt(1)
	v_mul_f32_e32 v159, s55, v163
	s_waitcnt lgkmcnt(0)
	v_mul_f32_e32 v155, s55, v169
	v_med3_f32 v157, v159, s47, v179
	v_med3_f32 v155, v155, s47, v179
	v_cvt_pk_fp8_f32 v221, v157, v155 op_sel:[0,0,1]
	ds_read2_b32 v[230:231], v181 offset0:8 offset1:16
	ds_read2_b32 v[232:233], v181 offset0:73 offset1:81
	ds_read2_b32 v[234:235], v181 offset0:138 offset1:146
	ds_read2_b32 v[236:237], v181 offset0:203 offset1:211
	v_mov_b64_e32 v[166:167], s[0:1]
	v_mad_u64_u32 v[228:229], s[6:7], s54, v134, v[166:167]
	v_lshl_add_u64 v[228:229], v[228:229], 0, v[136:137]
	s_waitcnt lgkmcnt(3)
	v_mul_f32_e32 v155, s55, v230
	s_waitcnt lgkmcnt(2)
	v_mul_f32_e32 v157, s55, v232
	global_store_dwordx2 v[228:229], v[220:221], off nt
	v_med3_f32 v155, v155, s47, v179
	v_med3_f32 v157, v157, s47, v179
	v_mov_b32_e32 v220, v133
	v_cvt_pk_fp8_f32 v220, v155, v157
	ds_read2_b32 v[228:229], v180 offset0:12 offset1:20
	ds_read2_b32 v[238:239], v180 offset0:77 offset1:85
	ds_read2_b32 v[240:241], v180 offset0:142 offset1:150
	s_waitcnt lgkmcnt(4)
	v_mul_f32_e32 v159, s55, v234
	s_waitcnt lgkmcnt(3)
	v_mul_f32_e32 v161, s55, v236
	v_med3_f32 v159, v159, s47, v179
	v_med3_f32 v155, v161, s47, v179
	ds_read2_b32 v[242:243], v180 offset0:207 offset1:215
	v_cvt_pk_fp8_f32 v220, v159, v155 op_sel:[0,0,1]
	s_waitcnt lgkmcnt(3)
	v_mul_f32_e32 v155, s55, v228
	s_waitcnt lgkmcnt(2)
	v_mul_f32_e32 v157, s55, v238
	v_med3_f32 v155, v155, s47, v179
	v_med3_f32 v157, v157, s47, v179
	v_mov_b32_e32 v221, v133
	v_cvt_pk_fp8_f32 v221, v155, v157
	s_waitcnt lgkmcnt(1)
	v_mul_f32_e32 v159, s55, v240
	s_waitcnt lgkmcnt(0)
	v_mul_f32_e32 v155, s55, v242
	v_med3_f32 v157, v159, s47, v179
	v_med3_f32 v155, v155, s47, v179
	v_cvt_pk_fp8_f32 v221, v157, v155 op_sel:[0,0,1]
	v_mad_u64_u32 v[244:245], s[6:7], s54, v138, v[166:167]
	v_lshl_add_u64 v[244:245], v[244:245], 0, v[136:137]
	v_mul_f32_e32 v155, s55, v231
	v_mul_f32_e32 v157, s55, v233
	global_store_dwordx2 v[244:245], v[220:221], off nt
	v_med3_f32 v155, v155, s47, v179
	v_med3_f32 v157, v157, s47, v179
	v_mov_b32_e32 v220, v133
	v_cvt_pk_fp8_f32 v220, v155, v157
	v_mul_f32_e32 v159, s55, v235
	v_mul_f32_e32 v155, s55, v237
	v_med3_f32 v157, v159, s47, v179
	v_med3_f32 v155, v155, s47, v179
	v_cvt_pk_fp8_f32 v220, v157, v155 op_sel:[0,0,1]
	v_mul_f32_e32 v155, s55, v229
	v_mul_f32_e32 v157, s55, v239
	v_med3_f32 v155, v155, s47, v179
	v_med3_f32 v157, v157, s47, v179
	v_mov_b32_e32 v221, v133
	v_cvt_pk_fp8_f32 v221, v155, v157
	v_mul_f32_e32 v159, s55, v241
	v_mul_f32_e32 v155, s55, v243
	v_med3_f32 v157, v159, s47, v179
	v_med3_f32 v155, v155, s47, v179
	v_cvt_pk_fp8_f32 v221, v157, v155 op_sel:[0,0,1]
	ds_read2_b32 v[230:231], v181 offset0:24 offset1:32
	ds_read2_b32 v[232:233], v181 offset0:89 offset1:97
	ds_read2_b32 v[234:235], v181 offset0:154 offset1:162
	ds_read2_b32 v[236:237], v181 offset0:219 offset1:227
	v_mad_u64_u32 v[228:229], s[6:7], s54, v140, v[166:167]
	v_lshl_add_u64 v[228:229], v[228:229], 0, v[136:137]
	s_waitcnt lgkmcnt(3)
	v_mul_f32_e32 v155, s55, v230
	s_waitcnt lgkmcnt(2)
	v_mul_f32_e32 v157, s55, v232
	global_store_dwordx2 v[228:229], v[220:221], off nt
	v_med3_f32 v155, v155, s47, v179
	v_med3_f32 v157, v157, s47, v179
	v_mov_b32_e32 v220, v133
	v_cvt_pk_fp8_f32 v220, v155, v157
	ds_read2_b32 v[228:229], v180 offset0:28 offset1:36
	ds_read2_b32 v[238:239], v180 offset0:93 offset1:101
	ds_read2_b32 v[240:241], v180 offset0:158 offset1:166
	s_waitcnt lgkmcnt(4)
	v_mul_f32_e32 v159, s55, v234
	s_waitcnt lgkmcnt(3)
	v_mul_f32_e32 v161, s55, v236
	v_med3_f32 v159, v159, s47, v179
	v_med3_f32 v155, v161, s47, v179
	ds_read2_b32 v[242:243], v180 offset0:223 offset1:231
	v_cvt_pk_fp8_f32 v220, v159, v155 op_sel:[0,0,1]
	s_waitcnt lgkmcnt(3)
	v_mul_f32_e32 v155, s55, v228
	s_waitcnt lgkmcnt(2)
	v_mul_f32_e32 v157, s55, v238
	v_med3_f32 v155, v155, s47, v179
	v_med3_f32 v157, v157, s47, v179
	v_mov_b32_e32 v221, v133
	v_cvt_pk_fp8_f32 v221, v155, v157
	s_waitcnt lgkmcnt(1)
	v_mul_f32_e32 v159, s55, v240
	s_waitcnt lgkmcnt(0)
	v_mul_f32_e32 v155, s55, v242
	v_med3_f32 v157, v159, s47, v179
	v_med3_f32 v155, v155, s47, v179
	v_cvt_pk_fp8_f32 v221, v157, v155 op_sel:[0,0,1]
	v_mad_u64_u32 v[244:245], s[6:7], s54, v142, v[166:167]
	v_lshl_add_u64 v[244:245], v[244:245], 0, v[136:137]
	v_mul_f32_e32 v155, s55, v231
	v_mul_f32_e32 v157, s55, v233
	global_store_dwordx2 v[244:245], v[220:221], off nt
	v_med3_f32 v155, v155, s47, v179
	v_med3_f32 v157, v157, s47, v179
	v_mov_b32_e32 v220, v133
	v_cvt_pk_fp8_f32 v220, v155, v157
	v_mul_f32_e32 v159, s55, v235
	v_mul_f32_e32 v155, s55, v237
	v_med3_f32 v157, v159, s47, v179
	v_med3_f32 v155, v155, s47, v179
	v_cvt_pk_fp8_f32 v220, v157, v155 op_sel:[0,0,1]
	v_mul_f32_e32 v155, s55, v229
	v_mul_f32_e32 v157, s55, v239
	v_med3_f32 v155, v155, s47, v179
	v_med3_f32 v157, v157, s47, v179
	v_mov_b32_e32 v221, v133
	v_cvt_pk_fp8_f32 v221, v155, v157
	v_mul_f32_e32 v159, s55, v241
	v_mul_f32_e32 v155, s55, v243
	v_med3_f32 v157, v159, s47, v179
	v_med3_f32 v155, v155, s47, v179
	v_cvt_pk_fp8_f32 v221, v157, v155 op_sel:[0,0,1]
	ds_read2_b32 v[230:231], v181 offset0:40 offset1:48
	ds_read2_b32 v[232:233], v181 offset0:105 offset1:113
	ds_read2_b32 v[234:235], v181 offset0:170 offset1:178
	ds_read2_b32 v[236:237], v181 offset0:235 offset1:243
	v_mad_u64_u32 v[228:229], s[6:7], s54, v144, v[166:167]
	v_lshl_add_u64 v[228:229], v[228:229], 0, v[136:137]
	s_waitcnt lgkmcnt(3)
	v_mul_f32_e32 v155, s55, v230
	s_waitcnt lgkmcnt(2)
	v_mul_f32_e32 v157, s55, v232
	global_store_dwordx2 v[228:229], v[220:221], off nt
	v_med3_f32 v155, v155, s47, v179
	v_med3_f32 v157, v157, s47, v179
	v_mov_b32_e32 v220, v133
	v_cvt_pk_fp8_f32 v220, v155, v157
	ds_read2_b32 v[228:229], v180 offset0:44 offset1:52
	ds_read2_b32 v[238:239], v180 offset0:109 offset1:117
	ds_read2_b32 v[240:241], v180 offset0:174 offset1:182
	s_waitcnt lgkmcnt(4)
	v_mul_f32_e32 v159, s55, v234
	s_waitcnt lgkmcnt(3)
	v_mul_f32_e32 v161, s55, v236
	v_med3_f32 v159, v159, s47, v179
	v_med3_f32 v155, v161, s47, v179
	ds_read2_b32 v[242:243], v180 offset0:239 offset1:247
	v_cvt_pk_fp8_f32 v220, v159, v155 op_sel:[0,0,1]
	s_waitcnt lgkmcnt(3)
	v_mul_f32_e32 v155, s55, v228
	s_waitcnt lgkmcnt(2)
	v_mul_f32_e32 v157, s55, v238
	v_med3_f32 v155, v155, s47, v179
	v_med3_f32 v157, v157, s47, v179
	v_mov_b32_e32 v221, v133
	v_cvt_pk_fp8_f32 v221, v155, v157
	s_waitcnt lgkmcnt(1)
	v_mul_f32_e32 v159, s55, v240
	s_waitcnt lgkmcnt(0)
	v_mul_f32_e32 v155, s55, v242
	v_med3_f32 v157, v159, s47, v179
	v_med3_f32 v155, v155, s47, v179
	v_cvt_pk_fp8_f32 v221, v157, v155 op_sel:[0,0,1]
	v_mad_u64_u32 v[244:245], s[6:7], s54, v146, v[166:167]
	v_lshl_add_u64 v[244:245], v[244:245], 0, v[136:137]
	v_mul_f32_e32 v155, s55, v231
	v_mul_f32_e32 v157, s55, v233
	global_store_dwordx2 v[244:245], v[220:221], off nt
	v_med3_f32 v155, v155, s47, v179
	v_med3_f32 v157, v157, s47, v179
	v_mov_b32_e32 v220, v133
	v_cvt_pk_fp8_f32 v220, v155, v157
	v_mul_f32_e32 v159, s55, v235
	v_mul_f32_e32 v155, s55, v237
	v_med3_f32 v157, v159, s47, v179
	v_med3_f32 v155, v155, s47, v179
	v_cvt_pk_fp8_f32 v220, v157, v155 op_sel:[0,0,1]
	v_mul_f32_e32 v155, s55, v229
	v_mul_f32_e32 v157, s55, v239
	v_med3_f32 v155, v155, s47, v179
	v_med3_f32 v157, v157, s47, v179
	v_mov_b32_e32 v221, v133
	v_cvt_pk_fp8_f32 v221, v155, v157
	v_mul_f32_e32 v159, s55, v241
	v_mul_f32_e32 v155, s55, v243
	v_med3_f32 v157, v159, s47, v179
	v_med3_f32 v155, v155, s47, v179
	v_cvt_pk_fp8_f32 v221, v157, v155 op_sel:[0,0,1]
	v_mul_f32_e32 v154, s55, v154
	v_mul_f32_e32 v155, s55, v156
	v_med3_f32 v157, v154, s47, v179
	v_med3_f32 v155, v155, s47, v179
	v_mov_b32_e32 v154, v133
	v_cvt_pk_fp8_f32 v154, v157, v155
	v_mul_f32_e32 v156, s55, v158
	v_mul_f32_e32 v155, s55, v164
	v_med3_f32 v156, v156, s47, v179
	v_med3_f32 v155, v155, s47, v179
	ds_read_b32 v158, v177 offset:18428
	v_cvt_pk_fp8_f32 v154, v156, v155 op_sel:[0,0,1]
	v_mul_f32_e32 v155, s55, v160
	v_mul_f32_e32 v156, s55, v162
	v_med3_f32 v159, v155, s47, v179
	v_med3_f32 v156, v156, s47, v179
	v_mov_b32_e32 v155, v133
	v_cvt_pk_fp8_f32 v155, v159, v156
	v_mul_f32_e32 v157, s55, v168
	s_waitcnt lgkmcnt(0)
	v_mul_f32_e32 v156, s55, v158
	v_med3_f32 v157, v157, s47, v179
	v_med3_f32 v156, v156, s47, v179
	v_cvt_pk_fp8_f32 v155, v157, v156 op_sel:[0,0,1]
	v_mad_u64_u32 v[228:229], s[6:7], s54, v148, v[166:167]
	v_mad_u64_u32 v[156:157], s[6:7], s54, v150, v[166:167]
	v_lshl_add_u64 v[228:229], v[228:229], 0, v[136:137]
	v_lshl_add_u64 v[156:157], v[156:157], 0, v[136:137]
	global_store_dwordx2 v[228:229], v[220:221], off nt
	global_store_dwordx2 v[156:157], v[154:155], off nt
	s_cbranch_execnz .LBB0_1735

.LBB0_1769:
	s_waitcnt vmcnt(31)
	ds_write2_b32 v183, v62, v63 offset1:1
	ds_write2_b32 v184, v64, v65 offset1:1
	s_waitcnt vmcnt(30)
	ds_write2_b32 v185, v58, v59 offset1:1
	ds_write2_b32 v186, v60, v61 offset1:1
	s_waitcnt vmcnt(29)
	ds_write2_b32 v187, v78, v79 offset1:1
	ds_write2_b32 v188, v80, v81 offset1:1
	s_waitcnt vmcnt(28)
	ds_write2_b32 v189, v74, v75 offset1:1
	ds_write2_b32 v190, v76, v77 offset1:1
	s_waitcnt vmcnt(27)
	ds_write2_b32 v191, v86, v87 offset1:1
	ds_write2_b32 v192, v88, v89 offset1:1
	s_waitcnt vmcnt(26)
	ds_write2_b32 v193, v82, v83 offset1:1
	ds_write2_b32 v195, v84, v85 offset1:1
	s_waitcnt vmcnt(25)
	ds_write2_b32 v199, v94, v95 offset1:1
	ds_write2_b32 v201, v96, v97 offset1:1
	s_waitcnt vmcnt(24)
	ds_write2_b32 v202, v90, v91 offset1:1
	ds_write2_b32 v203, v92, v93 offset1:1
	s_waitcnt vmcnt(23)
	ds_write2_b32 v204, v102, v103 offset1:1
	ds_write2_b32 v205, v104, v105 offset1:1
	s_waitcnt vmcnt(22)
	ds_write2_b32 v206, v98, v99 offset1:1
	ds_write2_b32 v207, v100, v101 offset1:1
	s_waitcnt vmcnt(21)
	ds_write2_b32 v208, v110, v111 offset1:1
	ds_write2_b32 v209, v112, v113 offset1:1
	s_waitcnt vmcnt(20)
	ds_write2_b32 v210, v106, v107 offset1:1
	ds_write2_b32 v211, v108, v109 offset1:1
	s_waitcnt vmcnt(19)
	ds_write2_b32 v212, v118, v119 offset1:1
	ds_write2_b32 v213, v120, v121 offset1:1
	s_waitcnt vmcnt(18)
	ds_write2_b32 v214, v114, v115 offset1:1
	ds_write2_b32 v215, v116, v117 offset1:1
	s_waitcnt vmcnt(17)
	ds_write2_b32 v216, v126, v127 offset1:1
	ds_write2_b32 v217, v128, v129 offset1:1
	s_waitcnt vmcnt(16)
	ds_write2_b32 v218, v122, v123 offset1:1
	ds_write2_b32 v219, v124, v125 offset1:1
	s_waitcnt lgkmcnt(0)
	s_waitcnt lgkmcnt(14)
	ds_read_b32 v132, v177 offset:16384
	v_cmp_eq_f32_e64 s[4:5], s57, 0
	s_and_b64 vcc, exec, s[4:5]
	s_cbranch_vccnz .LBB0_1771
	ds_read2_b32 v[154:155], v181 offset0:56 offset1:65
	ds_read2_b32 v[156:157], v181 offset0:121 offset1:130
	ds_read2_b32 v[158:159], v181 offset0:186 offset1:195
	s_waitcnt lgkmcnt(3)
	v_mul_f32_e32 v160, s57, v132
	v_med3_f32 v160, v160, s47, v179
	s_waitcnt lgkmcnt(2)
	v_mul_f32_e32 v155, s57, v155
	v_med3_f32 v155, v155, s47, v179
	v_mov_b32_e32 v184, v133
	v_cvt_pk_fp8_f32 v184, v160, v155
	ds_read2_b32 v[164:165], v182 offset0:123 offset1:132
	ds_read2_b32 v[160:161], v180 offset0:60 offset1:69
	ds_read2_b32 v[162:163], v180 offset0:125 offset1:134
	s_waitcnt lgkmcnt(4)
	v_mul_f32_e32 v157, s57, v157
	s_waitcnt lgkmcnt(3)
	v_mul_f32_e32 v159, s57, v159
	v_med3_f32 v157, v157, s47, v179
	v_med3_f32 v155, v159, s47, v179
	ds_read2_b32 v[168:169], v180 offset0:190 offset1:199
	v_cvt_pk_fp8_f32 v184, v157, v155 op_sel:[0,0,1]
	s_waitcnt lgkmcnt(3)
	v_mul_f32_e32 v155, s57, v165
	s_waitcnt lgkmcnt(2)
	v_mul_f32_e32 v157, s57, v161
	v_med3_f32 v155, v155, s47, v179
	v_med3_f32 v157, v157, s47, v179
	v_mov_b32_e32 v185, v133
	v_cvt_pk_fp8_f32 v185, v155, v157
	s_waitcnt lgkmcnt(1)
	v_mul_f32_e32 v159, s57, v163
	s_waitcnt lgkmcnt(0)
	v_mul_f32_e32 v155, s57, v169
	v_med3_f32 v157, v159, s47, v179
	v_med3_f32 v155, v155, s47, v179
	v_cvt_pk_fp8_f32 v185, v157, v155 op_sel:[0,0,1]
	ds_read2_b32 v[188:189], v181 offset0:8 offset1:16
	ds_read2_b32 v[190:191], v181 offset0:73 offset1:81
	ds_read2_b32 v[192:193], v181 offset0:138 offset1:146
	ds_read2_b32 v[202:203], v181 offset0:203 offset1:211
	v_mov_b64_e32 v[166:167], s[2:3]
	v_mad_u64_u32 v[186:187], s[4:5], s56, v134, v[166:167]
	v_lshl_add_u64 v[186:187], v[186:187], 0, v[136:137]
	s_waitcnt lgkmcnt(3)
	v_mul_f32_e32 v155, s57, v188
	s_waitcnt lgkmcnt(2)
	v_mul_f32_e32 v157, s57, v190
	global_store_dwordx2 v[186:187], v[184:185], off nt
	v_med3_f32 v155, v155, s47, v179
	v_med3_f32 v157, v157, s47, v179
	v_mov_b32_e32 v184, v133
	v_cvt_pk_fp8_f32 v184, v155, v157
	ds_read2_b32 v[186:187], v180 offset0:12 offset1:20
	ds_read2_b32 v[204:205], v180 offset0:77 offset1:85
	ds_read2_b32 v[206:207], v180 offset0:142 offset1:150
	s_waitcnt lgkmcnt(4)
	v_mul_f32_e32 v159, s57, v192
	s_waitcnt lgkmcnt(3)
	v_mul_f32_e32 v161, s57, v202
	v_med3_f32 v159, v159, s47, v179
	v_med3_f32 v155, v161, s47, v179
	ds_read2_b32 v[208:209], v180 offset0:207 offset1:215
	v_cvt_pk_fp8_f32 v184, v159, v155 op_sel:[0,0,1]
	s_waitcnt lgkmcnt(3)
	v_mul_f32_e32 v155, s57, v186
	s_waitcnt lgkmcnt(2)
	v_mul_f32_e32 v157, s57, v204
	v_med3_f32 v155, v155, s47, v179
	v_med3_f32 v157, v157, s47, v179
	v_mov_b32_e32 v185, v133
	v_cvt_pk_fp8_f32 v185, v155, v157
	s_waitcnt lgkmcnt(1)
	v_mul_f32_e32 v159, s57, v206
	s_waitcnt lgkmcnt(0)
	v_mul_f32_e32 v155, s57, v208
	v_med3_f32 v157, v159, s47, v179
	v_med3_f32 v155, v155, s47, v179
	v_cvt_pk_fp8_f32 v185, v157, v155 op_sel:[0,0,1]
	v_mad_u64_u32 v[210:211], s[4:5], s56, v138, v[166:167]
	v_lshl_add_u64 v[210:211], v[210:211], 0, v[136:137]
	v_mul_f32_e32 v155, s57, v189
	v_mul_f32_e32 v157, s57, v191
	global_store_dwordx2 v[210:211], v[184:185], off nt
	v_med3_f32 v155, v155, s47, v179
	v_med3_f32 v157, v157, s47, v179
	v_mov_b32_e32 v184, v133
	v_cvt_pk_fp8_f32 v184, v155, v157
	v_mul_f32_e32 v159, s57, v193
	v_mul_f32_e32 v155, s57, v203
	v_med3_f32 v157, v159, s47, v179
	v_med3_f32 v155, v155, s47, v179
	v_cvt_pk_fp8_f32 v184, v157, v155 op_sel:[0,0,1]
	v_mul_f32_e32 v155, s57, v187
	v_mul_f32_e32 v157, s57, v205
	v_med3_f32 v155, v155, s47, v179
	v_med3_f32 v157, v157, s47, v179
	v_mov_b32_e32 v185, v133
	v_cvt_pk_fp8_f32 v185, v155, v157
	v_mul_f32_e32 v159, s57, v207
	v_mul_f32_e32 v155, s57, v209
	v_med3_f32 v157, v159, s47, v179
	v_med3_f32 v155, v155, s47, v179
	v_cvt_pk_fp8_f32 v185, v157, v155 op_sel:[0,0,1]
	ds_read2_b32 v[188:189], v181 offset0:24 offset1:32
	ds_read2_b32 v[190:191], v181 offset0:89 offset1:97
	ds_read2_b32 v[192:193], v181 offset0:154 offset1:162
	ds_read2_b32 v[202:203], v181 offset0:219 offset1:227
	v_mad_u64_u32 v[186:187], s[4:5], s56, v140, v[166:167]
	v_lshl_add_u64 v[186:187], v[186:187], 0, v[136:137]
	s_waitcnt lgkmcnt(3)
	v_mul_f32_e32 v155, s57, v188
	s_waitcnt lgkmcnt(2)
	v_mul_f32_e32 v157, s57, v190
	global_store_dwordx2 v[186:187], v[184:185], off nt
	v_med3_f32 v155, v155, s47, v179
	v_med3_f32 v157, v157, s47, v179
	v_mov_b32_e32 v184, v133
	v_cvt_pk_fp8_f32 v184, v155, v157
	ds_read2_b32 v[186:187], v180 offset0:28 offset1:36
	ds_read2_b32 v[204:205], v180 offset0:93 offset1:101
	ds_read2_b32 v[206:207], v180 offset0:158 offset1:166
	s_waitcnt lgkmcnt(4)
	v_mul_f32_e32 v159, s57, v192
	s_waitcnt lgkmcnt(3)
	v_mul_f32_e32 v161, s57, v202
	v_med3_f32 v159, v159, s47, v179
	v_med3_f32 v155, v161, s47, v179
	ds_read2_b32 v[208:209], v180 offset0:223 offset1:231
	v_cvt_pk_fp8_f32 v184, v159, v155 op_sel:[0,0,1]
	s_waitcnt lgkmcnt(3)
	v_mul_f32_e32 v155, s57, v186
	s_waitcnt lgkmcnt(2)
	v_mul_f32_e32 v157, s57, v204
	v_med3_f32 v155, v155, s47, v179
	v_med3_f32 v157, v157, s47, v179
	v_mov_b32_e32 v185, v133
	v_cvt_pk_fp8_f32 v185, v155, v157
	s_waitcnt lgkmcnt(1)
	v_mul_f32_e32 v159, s57, v206
	s_waitcnt lgkmcnt(0)
	v_mul_f32_e32 v155, s57, v208
	v_med3_f32 v157, v159, s47, v179
	v_med3_f32 v155, v155, s47, v179
	v_cvt_pk_fp8_f32 v185, v157, v155 op_sel:[0,0,1]
	v_mad_u64_u32 v[210:211], s[4:5], s56, v142, v[166:167]
	v_lshl_add_u64 v[210:211], v[210:211], 0, v[136:137]
	v_mul_f32_e32 v155, s57, v189
	v_mul_f32_e32 v157, s57, v191
	global_store_dwordx2 v[210:211], v[184:185], off nt
	v_med3_f32 v155, v155, s47, v179
	v_med3_f32 v157, v157, s47, v179
	v_mov_b32_e32 v184, v133
	v_cvt_pk_fp8_f32 v184, v155, v157
	v_mul_f32_e32 v159, s57, v193
	v_mul_f32_e32 v155, s57, v203
	v_med3_f32 v157, v159, s47, v179
	v_med3_f32 v155, v155, s47, v179
	v_cvt_pk_fp8_f32 v184, v157, v155 op_sel:[0,0,1]
	v_mul_f32_e32 v155, s57, v187
	v_mul_f32_e32 v157, s57, v205
	v_med3_f32 v155, v155, s47, v179
	v_med3_f32 v157, v157, s47, v179
	v_mov_b32_e32 v185, v133
	v_cvt_pk_fp8_f32 v185, v155, v157
	v_mul_f32_e32 v159, s57, v207
	v_mul_f32_e32 v155, s57, v209
	v_med3_f32 v157, v159, s47, v179
	v_med3_f32 v155, v155, s47, v179
	v_cvt_pk_fp8_f32 v185, v157, v155 op_sel:[0,0,1]
	ds_read2_b32 v[188:189], v181 offset0:40 offset1:48
	ds_read2_b32 v[190:191], v181 offset0:105 offset1:113
	ds_read2_b32 v[192:193], v181 offset0:170 offset1:178
	ds_read2_b32 v[202:203], v181 offset0:235 offset1:243
	v_mad_u64_u32 v[186:187], s[4:5], s56, v144, v[166:167]
	v_lshl_add_u64 v[186:187], v[186:187], 0, v[136:137]
	s_waitcnt lgkmcnt(3)
	v_mul_f32_e32 v155, s57, v188
	s_waitcnt lgkmcnt(2)
	v_mul_f32_e32 v157, s57, v190
	global_store_dwordx2 v[186:187], v[184:185], off nt
	v_med3_f32 v155, v155, s47, v179
	v_med3_f32 v157, v157, s47, v179
	v_mov_b32_e32 v184, v133
	v_cvt_pk_fp8_f32 v184, v155, v157
	ds_read2_b32 v[186:187], v180 offset0:44 offset1:52
	ds_read2_b32 v[204:205], v180 offset0:109 offset1:117
	ds_read2_b32 v[206:207], v180 offset0:174 offset1:182
	s_waitcnt lgkmcnt(4)
	v_mul_f32_e32 v159, s57, v192
	s_waitcnt lgkmcnt(3)
	v_mul_f32_e32 v161, s57, v202
	v_med3_f32 v159, v159, s47, v179
	v_med3_f32 v155, v161, s47, v179
	ds_read2_b32 v[208:209], v180 offset0:239 offset1:247
	v_cvt_pk_fp8_f32 v184, v159, v155 op_sel:[0,0,1]
	s_waitcnt lgkmcnt(3)
	v_mul_f32_e32 v155, s57, v186
	s_waitcnt lgkmcnt(2)
	v_mul_f32_e32 v157, s57, v204
	v_med3_f32 v155, v155, s47, v179
	v_med3_f32 v157, v157, s47, v179
	v_mov_b32_e32 v185, v133
	v_cvt_pk_fp8_f32 v185, v155, v157
	s_waitcnt lgkmcnt(1)
	v_mul_f32_e32 v159, s57, v206
	s_waitcnt lgkmcnt(0)
	v_mul_f32_e32 v155, s57, v208
	v_med3_f32 v157, v159, s47, v179
	v_med3_f32 v155, v155, s47, v179
	v_cvt_pk_fp8_f32 v185, v157, v155 op_sel:[0,0,1]
	v_mad_u64_u32 v[210:211], s[4:5], s56, v146, v[166:167]
	v_lshl_add_u64 v[210:211], v[210:211], 0, v[136:137]
	v_mul_f32_e32 v155, s57, v189
	v_mul_f32_e32 v157, s57, v191
	global_store_dwordx2 v[210:211], v[184:185], off nt
	v_med3_f32 v155, v155, s47, v179
	v_med3_f32 v157, v157, s47, v179
	v_mov_b32_e32 v184, v133
	v_cvt_pk_fp8_f32 v184, v155, v157
	v_mul_f32_e32 v159, s57, v193
	v_mul_f32_e32 v155, s57, v203
	v_med3_f32 v157, v159, s47, v179
	v_med3_f32 v155, v155, s47, v179
	v_cvt_pk_fp8_f32 v184, v157, v155 op_sel:[0,0,1]
	v_mul_f32_e32 v155, s57, v187
	v_mul_f32_e32 v157, s57, v205
	v_med3_f32 v155, v155, s47, v179
	v_med3_f32 v157, v157, s47, v179
	v_mov_b32_e32 v185, v133
	v_cvt_pk_fp8_f32 v185, v155, v157
	v_mul_f32_e32 v159, s57, v207
	v_mul_f32_e32 v155, s57, v209
	v_med3_f32 v157, v159, s47, v179
	v_med3_f32 v155, v155, s47, v179
	v_cvt_pk_fp8_f32 v185, v157, v155 op_sel:[0,0,1]
	v_mul_f32_e32 v154, s57, v154
	v_mul_f32_e32 v155, s57, v156
	v_med3_f32 v157, v154, s47, v179
	v_med3_f32 v155, v155, s47, v179
	v_mov_b32_e32 v154, v133
	v_cvt_pk_fp8_f32 v154, v157, v155
	v_mul_f32_e32 v156, s57, v158
	v_mul_f32_e32 v155, s57, v164
	v_med3_f32 v156, v156, s47, v179
	v_med3_f32 v155, v155, s47, v179
	ds_read_b32 v158, v177 offset:18428
	v_cvt_pk_fp8_f32 v154, v156, v155 op_sel:[0,0,1]
	v_mul_f32_e32 v155, s57, v160
	v_mul_f32_e32 v156, s57, v162
	v_med3_f32 v159, v155, s47, v179
	v_med3_f32 v156, v156, s47, v179
	v_mov_b32_e32 v155, v133
	v_cvt_pk_fp8_f32 v155, v159, v156
	v_mul_f32_e32 v157, s57, v168
	s_waitcnt lgkmcnt(0)
	v_mul_f32_e32 v156, s57, v158
	v_med3_f32 v157, v157, s47, v179
	v_med3_f32 v156, v156, s47, v179
	v_cvt_pk_fp8_f32 v155, v157, v156 op_sel:[0,0,1]
	v_mad_u64_u32 v[186:187], s[4:5], s56, v148, v[166:167]
	v_mad_u64_u32 v[156:157], s[4:5], s56, v150, v[166:167]
	v_lshl_add_u64 v[186:187], v[186:187], 0, v[136:137]
	v_lshl_add_u64 v[156:157], v[156:157], 0, v[136:137]
	global_store_dwordx2 v[186:187], v[184:185], off nt
	global_store_dwordx2 v[156:157], v[154:155], off nt
	s_cbranch_execnz .LBB0_1701
	s_branch .LBB0_1700
